# LN+router phases: xor-butterfly reductions via DPP instead of ds_bpermute
# baseline (speedup 1.0000x reference)
.LBB0_1290:
	s_waitcnt vmcnt(0)
	v_lshlrev_b32_e32 v92, 16, v86
	v_and_b32_e32 v93, 0xffff0000, v86
	v_lshlrev_b32_e32 v98, 16, v87
	v_and_b32_e32 v99, 0xffff0000, v87
	v_add_f32_e32 v86, v92, v93
	v_add_f32_e32 v87, v98, v99
	v_lshlrev_b32_e32 v100, 16, v84
	v_and_b32_e32 v101, 0xffff0000, v84
	v_lshlrev_b32_e32 v102, 16, v85
	v_and_b32_e32 v103, 0xffff0000, v85
	v_add_f32_e32 v86, v86, v87
	v_add_f32_e32 v84, v100, v101
	v_add_f32_e32 v85, v102, v103
	v_lshlrev_b32_e32 v104, 16, v82
	v_and_b32_e32 v105, 0xffff0000, v82
	v_lshlrev_b32_e32 v106, 16, v83
	v_and_b32_e32 v107, 0xffff0000, v83
	v_add_f32_e32 v86, 0, v86
	v_add_f32_e32 v84, v84, v85
	v_add_f32_e32 v82, v104, v105
	v_add_f32_e32 v83, v106, v107
	v_lshlrev_b32_e32 v94, 16, v80
	v_and_b32_e32 v95, 0xffff0000, v80
	v_lshlrev_b32_e32 v96, 16, v81
	v_and_b32_e32 v97, 0xffff0000, v81
	v_add_f32_e32 v84, v86, v84
	v_add_f32_e32 v82, v82, v83
	v_add_f32_e32 v80, v94, v95
	v_add_f32_e32 v81, v96, v97
	v_lshlrev_b32_e32 v86, 16, v76
	v_and_b32_e32 v87, 0xffff0000, v76
	v_lshlrev_b32_e32 v88, 16, v77
	v_and_b32_e32 v89, 0xffff0000, v77
	v_add_f32_e32 v82, v84, v82
	v_add_f32_e32 v80, v80, v81
	v_add_f32_e32 v76, v86, v87
	v_add_f32_e32 v77, v88, v89
	v_add_f32_e32 v80, v82, v80
	v_add_f32_e32 v76, v76, v77
	v_add_f32_e32 v76, v80, v76
	v_lshlrev_b32_e32 v80, 16, v72
	v_and_b32_e32 v81, 0xffff0000, v72
	v_lshlrev_b32_e32 v82, 16, v73
	v_and_b32_e32 v83, 0xffff0000, v73
	v_add_f32_e32 v72, v80, v81
	v_add_f32_e32 v73, v82, v83
	v_add_f32_e32 v72, v72, v73
	v_add_f32_e32 v76, v76, v72
	v_lshlrev_b32_e32 v72, 16, v74
	v_and_b32_e32 v73, 0xffff0000, v74
	v_lshlrev_b32_e32 v74, 16, v75
	v_and_b32_e32 v75, 0xffff0000, v75
	v_add_f32_e32 v77, v72, v73
	v_add_f32_e32 v84, v74, v75
	v_add_f32_e32 v77, v77, v84
	v_add_f32_e32 v84, v76, v77
	v_lshlrev_b32_e32 v76, 16, v78
	v_and_b32_e32 v77, 0xffff0000, v78
	v_lshlrev_b32_e32 v78, 16, v79
	v_and_b32_e32 v79, 0xffff0000, v79
	v_add_f32_e32 v85, v76, v77
	v_add_f32_e32 v90, v78, v79
	v_add_f32_e32 v85, v85, v90
	v_add_f32_e32 v84, v84, v85
	s_mov_b32 s0, 0x800000
	v_mov_b32_e32 v176, 0
	s_add_i32 s22, s30, 8
	s_cmp_gt_u32 s30, 25
	s_waitcnt lgkmcnt(0)
	s_nop 1
	v_add_f32_dpp v84, v84, v84 quad_perm:[1,0,3,2] row_mask:0xf bank_mask:0xf
	s_waitcnt lgkmcnt(0)
	s_nop 1
	v_add_f32_dpp v84, v84, v84 quad_perm:[2,3,0,1] row_mask:0xf bank_mask:0xf
	s_waitcnt lgkmcnt(0)
	s_nop 1
	v_add_f32_dpp v84, v84, v84 row_half_mirror row_mask:0xf bank_mask:0xf
	s_waitcnt lgkmcnt(0)
	s_nop 1
	v_add_f32_dpp v84, v84, v84 row_mirror row_mask:0xf bank_mask:0xf
	ds_bpermute_b32 v85, v111, v84
	s_waitcnt lgkmcnt(0)
	v_add_f32_e32 v84, v84, v85
	ds_bpermute_b32 v85, v112, v84
	s_waitcnt lgkmcnt(0)
	v_add_f32_e32 v90, v84, v85
	v_fmac_f32_e32 v93, 0xba000000, v90
	v_fmac_f32_e32 v101, 0xba000000, v90
	v_fmac_f32_e32 v99, 0xba000000, v90
	v_fmac_f32_e32 v92, 0xba000000, v90
	v_fmac_f32_e32 v103, 0xba000000, v90
	v_fmac_f32_e32 v100, 0xba000000, v90
	v_mov_b32_e32 v140, v93
	v_mov_b32_e32 v141, v101
	v_fmac_f32_e32 v98, 0xba000000, v90
	v_fmac_f32_e32 v102, 0xba000000, v90
	v_mov_b32_e32 v84, v92
	v_mov_b32_e32 v85, v100
	v_pk_mul_f32 v[140:141], v[140:141], v[140:141]
	v_mov_b32_e32 v164, v99
	v_mov_b32_e32 v165, v103
	v_pk_fma_f32 v[84:85], v[84:85], v[84:85], v[140:141]
	v_mov_b32_e32 v140, v98
	v_mov_b32_e32 v141, v102
	v_pk_mul_f32 v[164:165], v[164:165], v[164:165]
	v_fmac_f32_e32 v105, 0xba000000, v90
	v_pk_fma_f32 v[140:141], v[140:141], v[140:141], v[164:165]
	v_fmac_f32_e32 v104, 0xba000000, v90
	v_pk_add_f32 v[84:85], v[84:85], v[140:141]
	v_fmac_f32_e32 v107, 0xba000000, v90
	v_fmac_f32_e32 v106, 0xba000000, v90
	v_pk_add_f32 v[84:85], v[84:85], v[84:85] op_sel_hi:[0,1]
	v_pk_mul_f32 v[140:141], v[106:107], v[106:107]
	v_pk_mul_f32 v[164:165], v[104:105], v[104:105]
	v_fmac_f32_e32 v94, 0xba000000, v90
	v_pk_mov_b32 v[166:167], v[164:165], v[140:141] op_sel:[1,0]
	v_mov_b32_e32 v165, v141
	v_fmac_f32_e32 v95, 0xba000000, v90
	v_fmac_f32_e32 v96, 0xba000000, v90
	v_mul_f32_e32 v84, v94, v94
	v_pk_add_f32 v[140:141], v[166:167], v[164:165]
	v_fmac_f32_e32 v97, 0xba000000, v90
	v_pk_fma_f32 v[164:165], v[94:95], v[94:95], v[84:85] op_sel_hi:[1,1,0]
	v_mul_f32_e32 v84, v96, v96
	v_pk_add_f32 v[140:141], v[140:141], v[140:141] op_sel_hi:[0,1]
	v_pk_fma_f32 v[166:167], v[96:97], v[96:97], v[84:85] op_sel_hi:[1,1,0]
	v_fmac_f32_e32 v89, 0xba000000, v90
	v_fmac_f32_e32 v88, 0xba000000, v90
	v_fmac_f32_e32 v87, 0xba000000, v90
	v_fmac_f32_e32 v86, 0xba000000, v90
	v_mul_f32_e32 v164, v86, v86
	v_mul_f32_e32 v166, v87, v87
	v_mul_f32_e32 v140, v88, v88
	v_mul_f32_e32 v84, v89, v89
	v_pk_add_f32 v[164:165], v[164:165], v[166:167]
	v_pk_add_f32 v[84:85], v[140:141], v[84:85]
	v_fmac_f32_e32 v81, 0xba000000, v90
	v_pk_add_f32 v[84:85], v[164:165], v[84:85]
	v_fmac_f32_e32 v80, 0xba000000, v90
	v_fmac_f32_e32 v83, 0xba000000, v90
	v_fmac_f32_e32 v82, 0xba000000, v90
	v_pk_add_f32 v[84:85], v[84:85], v[84:85] op_sel_hi:[0,1]
	v_pk_mul_f32 v[140:141], v[82:83], v[82:83]
	v_pk_mul_f32 v[172:173], v[80:81], v[80:81]
	v_fmac_f32_e32 v72, 0xba000000, v90
	v_pk_mov_b32 v[174:175], v[172:173], v[140:141] op_sel:[1,0]
	v_mov_b32_e32 v173, v141
	v_fmac_f32_e32 v73, 0xba000000, v90
	v_fmac_f32_e32 v74, 0xba000000, v90
	v_mul_f32_e32 v84, v72, v72
	v_pk_add_f32 v[140:141], v[174:175], v[172:173]
	v_fmac_f32_e32 v75, 0xba000000, v90
	v_pk_fma_f32 v[172:173], v[72:73], v[72:73], v[84:85] op_sel_hi:[1,1,0]
	v_mul_f32_e32 v84, v74, v74
	v_pk_add_f32 v[140:141], v[140:141], v[140:141] op_sel_hi:[0,1]
	v_pk_fma_f32 v[174:175], v[74:75], v[74:75], v[84:85] op_sel_hi:[1,1,0]
	v_fmac_f32_e32 v79, 0xba000000, v90
	v_fmac_f32_e32 v78, 0xba000000, v90
	v_fmac_f32_e32 v77, 0xba000000, v90
	v_fmac_f32_e32 v76, 0xba000000, v90
	v_mul_f32_e32 v172, v76, v76
	v_mul_f32_e32 v174, v77, v77
	v_mul_f32_e32 v140, v78, v78
	v_mul_f32_e32 v84, v79, v79
	v_pk_add_f32 v[172:173], v[172:173], v[174:175]
	v_pk_add_f32 v[84:85], v[140:141], v[84:85]
	s_nop 0
	v_pk_add_f32 v[84:85], v[172:173], v[84:85]
	s_nop 0
	v_add_f32_e32 v84, v84, v85
	s_waitcnt lgkmcnt(0)
	s_nop 1
	v_add_f32_dpp v84, v84, v84 quad_perm:[1,0,3,2] row_mask:0xf bank_mask:0xf
	s_waitcnt lgkmcnt(0)
	s_nop 1
	v_add_f32_dpp v84, v84, v84 quad_perm:[2,3,0,1] row_mask:0xf bank_mask:0xf
	s_waitcnt lgkmcnt(0)
	s_nop 1
	v_add_f32_dpp v84, v84, v84 row_half_mirror row_mask:0xf bank_mask:0xf
	s_waitcnt lgkmcnt(0)
	s_nop 1
	v_add_f32_dpp v84, v84, v84 row_mirror row_mask:0xf bank_mask:0xf
	ds_bpermute_b32 v85, v111, v84
	s_waitcnt lgkmcnt(0)
	v_add_f32_e32 v84, v84, v85
	ds_bpermute_b32 v85, v112, v84
	s_waitcnt lgkmcnt(0)
	v_add_f32_e32 v84, v84, v85
	v_fmamk_f32 v84, v84, 0x3a000000, v155
	v_mul_f32_e32 v85, 0x4b800000, v84
	v_cmp_gt_f32_e32 vcc, s0, v84
	s_mov_b64 s[0:1], 0x34000000
	s_nop 0
	v_cndmask_b32_e32 v84, v84, v85, vcc
	v_rsq_f32_e32 v90, v84
	v_lshl_add_u64 v[84:85], v[70:71], 0, s[0:1]
	s_mov_b32 s0, 0x38400000
	v_mul_f32_e32 v140, 0x45800000, v90
	v_cndmask_b32_e32 v90, v90, v140, vcc
	v_pk_mul_f32 v[92:93], v[92:93], v[90:91] op_sel_hi:[1,0]
	v_pk_mul_f32 v[98:99], v[98:99], v[90:91] op_sel_hi:[1,0]
	v_pk_fma_f32 v[92:93], v[196:197], v[92:93], v[200:201]
	v_pk_fma_f32 v[98:99], v[198:199], v[98:99], v[202:203]
	v_bfe_u32 v140, v92, 16, 1
	v_add3_u32 v140, v92, v140, s39
	v_bfe_u32 v141, v93, 16, 1
	v_lshrrev_b32_e32 v140, 16, v140
	v_add3_u32 v141, v93, v141, s39
	v_and_or_b32 v140, v141, s38, v140
	v_bfe_u32 v141, v98, 16, 1
	v_add3_u32 v141, v98, v141, s39
	v_bfe_u32 v163, v99, 16, 1
	v_lshrrev_b32_e32 v141, 16, v141
	v_add3_u32 v163, v99, v163, s39
	v_and_or_b32 v141, v163, s38, v141
	v_pk_fma_f32 v[92:93], v[6:7], v[92:93], v[2:3]
	global_store_dwordx2 v[84:85], v[140:141], off
	v_med3_f32 v84, v92, s40, v160
	v_med3_f32 v85, v93, s40, v160
	v_mov_b32_e32 v140, 0
	v_cvt_pk_fp8_f32 v140, v84, v85
	v_pk_fma_f32 v[98:99], v[8:9], v[98:99], v[4:5]
	v_pk_mul_f32 v[100:101], v[100:101], v[90:91] op_sel_hi:[1,0]
	v_med3_f32 v84, v98, s40, v160
	v_med3_f32 v85, v99, s40, v160
	v_cvt_pk_fp8_f32 v140, v84, v85 op_sel:[0,0,1]
	v_lshl_add_u64 v[84:85], s[92:93], 0, v[66:67]
	v_add_co_u32_e32 v84, vcc, s0, v84
	v_pk_mul_f32 v[102:103], v[102:103], v[90:91] op_sel_hi:[1,0]
	s_nop 0
	v_addc_co_u32_e32 v85, vcc, 0, v85, vcc
	global_store_dword v[84:85], v140, off
	s_mov_b64 s[0:1], 0x34000200
	v_lshl_add_u64 v[140:141], v[70:71], 0, s[0:1]
	v_pk_mul_f32 v[104:105], v[104:105], v[90:91] op_sel_hi:[1,0]
	v_pk_mul_f32 v[106:107], v[106:107], v[90:91] op_sel_hi:[1,0]
	s_mov_b64 s[0:1], 0x34000400
	v_pk_mul_f32 v[94:95], v[94:95], v[90:91] op_sel_hi:[1,0]
	v_pk_mul_f32 v[96:97], v[96:97], v[90:91] op_sel_hi:[1,0]
	v_pk_mul_f32 v[86:87], v[86:87], v[90:91] op_sel_hi:[1,0]
	v_pk_mul_f32 v[88:89], v[88:89], v[90:91] op_sel_hi:[1,0]
	v_pk_mul_f32 v[80:81], v[80:81], v[90:91] op_sel_hi:[1,0]
	v_pk_mul_f32 v[82:83], v[82:83], v[90:91] op_sel_hi:[1,0]
	v_pk_mul_f32 v[72:73], v[72:73], v[90:91] op_sel_hi:[1,0]
	v_pk_mul_f32 v[74:75], v[74:75], v[90:91] op_sel_hi:[1,0]
	v_pk_mul_f32 v[172:173], v[76:77], v[90:91] op_sel_hi:[1,0]
	v_and_b32_sdwa v76, v98, v159 dst_sel:DWORD dst_unused:UNUSED_PAD src0_sel:WORD_1 src1_sel:DWORD
	v_and_b32_sdwa v77, v92, v159 dst_sel:DWORD dst_unused:UNUSED_PAD src0_sel:WORD_1 src1_sel:DWORD
	v_pk_mul_f32 v[174:175], v[78:79], v[90:91] op_sel_hi:[1,0]
	v_add3_u32 v90, v92, v77, s39
	v_add3_u32 v92, v98, v76, s39
	v_and_b32_sdwa v78, v99, v159 dst_sel:DWORD dst_unused:UNUSED_PAD src0_sel:WORD_1 src1_sel:DWORD
	v_add3_u32 v98, v99, v78, s39
	v_and_b32_sdwa v79, v93, v159 dst_sel:DWORD dst_unused:UNUSED_PAD src0_sel:WORD_1 src1_sel:DWORD
	v_add3_u32 v93, v93, v79, s39
	v_and_b32_e32 v98, 0xffff0000, v98
	v_and_b32_e32 v99, 0xffff0000, v93
	v_or_b32_sdwa v93, v98, v92 dst_sel:DWORD dst_unused:UNUSED_PAD src0_sel:DWORD src1_sel:WORD_1
	v_or_b32_sdwa v92, v99, v90 dst_sel:DWORD dst_unused:UNUSED_PAD src0_sel:DWORD src1_sel:WORD_1
	v_pk_fma_f32 v[100:101], v[204:205], v[100:101], v[208:209]
	v_pk_fma_f32 v[166:167], v[206:207], v[102:103], v[210:211]
	v_bfe_u32 v102, v100, 16, 1
	v_add3_u32 v102, v100, v102, s39
	v_bfe_u32 v103, v101, 16, 1
	v_lshrrev_b32_e32 v102, 16, v102
	v_add3_u32 v103, v101, v103, s39
	v_and_or_b32 v164, v103, s38, v102
	v_bfe_u32 v102, v166, 16, 1
	v_add3_u32 v102, v166, v102, s39
	v_pk_fma_f32 v[100:101], v[14:15], v[100:101], v[10:11]
	v_lshrrev_b32_e32 v163, 16, v102
	v_med3_f32 v102, v100, s40, v160
	v_med3_f32 v103, v101, s40, v160
	v_mov_b32_e32 v168, 0
	v_cvt_pk_fp8_f32 v168, v102, v103
	v_pk_fma_f32 v[102:103], v[16:17], v[166:167], v[12:13]
	v_bfe_u32 v165, v167, 16, 1
	v_med3_f32 v166, v102, s40, v160
	v_med3_f32 v169, v103, s40, v160
	v_cvt_pk_fp8_f32 v168, v166, v169 op_sel:[0,0,1]
	v_add3_u32 v165, v167, v165, s39
	v_and_or_b32 v165, v165, s38, v163
	global_store_dwordx2 v[140:141], v[164:165], off
	global_store_dword v[84:85], v168, off offset:256
	v_mov_b32_e32 v163, 0
	v_lshl_add_u64 v[140:141], v[70:71], 0, s[0:1]
	s_mov_b64 s[0:1], 0x34000600
	v_and_b32_sdwa v98, v100, v159 dst_sel:DWORD dst_unused:UNUSED_PAD src0_sel:WORD_1 src1_sel:DWORD
	v_and_b32_sdwa v99, v103, v159 dst_sel:DWORD dst_unused:UNUSED_PAD src0_sel:WORD_1 src1_sel:DWORD
	v_and_b32_sdwa v90, v102, v159 dst_sel:DWORD dst_unused:UNUSED_PAD src0_sel:WORD_1 src1_sel:DWORD
	v_add3_u32 v98, v100, v98, s39
	v_add3_u32 v99, v103, v99, s39
	v_add3_u32 v90, v102, v90, s39
	v_and_b32_e32 v99, 0xffff0000, v99
	v_or_b32_sdwa v99, v99, v90 dst_sel:DWORD dst_unused:UNUSED_PAD src0_sel:DWORD src1_sel:WORD_1
	v_pk_fma_f32 v[164:165], v[214:215], v[104:105], v[218:219]
	v_pk_fma_f32 v[166:167], v[216:217], v[106:107], v[220:221]
	v_bfe_u32 v168, v164, 16, 1
	v_bfe_u32 v169, v165, 16, 1
	v_pk_fma_f32 v[106:107], v[22:23], v[164:165], v[18:19]
	v_add3_u32 v164, v164, v168, s39
	v_add3_u32 v165, v165, v169, s39
	v_med3_f32 v168, v106, s40, v160
	v_med3_f32 v169, v107, s40, v160
	v_cvt_pk_fp8_f32 v163, v168, v169
	v_bfe_u32 v170, v166, 16, 1
	v_pk_fma_f32 v[104:105], v[24:25], v[166:167], v[20:21]
	v_add3_u32 v166, v166, v170, s39
	v_med3_f32 v170, v104, s40, v160
	v_med3_f32 v168, v105, s40, v160
	v_bfe_u32 v171, v167, 16, 1
	v_cvt_pk_fp8_f32 v163, v170, v168 op_sel:[0,0,1]
	v_add3_u32 v167, v167, v171, s39
	v_lshrrev_b32_e32 v164, 16, v164
	v_lshrrev_b32_e32 v166, 16, v166
	v_and_or_b32 v164, v165, s38, v164
	v_and_or_b32 v165, v167, s38, v166
	global_store_dwordx2 v[140:141], v[164:165], off
	global_store_dword v[84:85], v163, off offset:512
	v_mov_b32_e32 v163, 0
	v_lshl_add_u64 v[140:141], v[70:71], 0, s[0:1]
	s_mov_b64 s[0:1], 0x34000800
	v_and_b32_sdwa v90, v104, v159 dst_sel:DWORD dst_unused:UNUSED_PAD src0_sel:WORD_1 src1_sel:DWORD
	v_add3_u32 v90, v104, v90, s39
	v_pk_fma_f32 v[164:165], v[222:223], v[94:95], v[226:227]
	v_pk_fma_f32 v[166:167], v[224:225], v[96:97], v[228:229]
	v_bfe_u32 v168, v164, 16, 1
	v_bfe_u32 v169, v165, 16, 1
	v_pk_fma_f32 v[96:97], v[30:31], v[164:165], v[26:27]
	v_add3_u32 v164, v164, v168, s39
	v_add3_u32 v165, v165, v169, s39
	v_med3_f32 v168, v96, s40, v160
	v_med3_f32 v169, v97, s40, v160
	v_cvt_pk_fp8_f32 v163, v168, v169
	v_bfe_u32 v170, v166, 16, 1
	v_pk_fma_f32 v[94:95], v[32:33], v[166:167], v[28:29]
	v_add3_u32 v166, v166, v170, s39
	v_med3_f32 v170, v94, s40, v160
	v_med3_f32 v168, v95, s40, v160
	v_bfe_u32 v171, v167, 16, 1
	v_cvt_pk_fp8_f32 v163, v170, v168 op_sel:[0,0,1]
	v_add3_u32 v167, v167, v171, s39
	v_lshrrev_b32_e32 v164, 16, v164
	v_lshrrev_b32_e32 v166, 16, v166
	v_and_or_b32 v164, v165, s38, v164
	v_and_or_b32 v165, v167, s38, v166
	global_store_dwordx2 v[140:141], v[164:165], off
	global_store_dword v[84:85], v163, off offset:768
	v_mov_b32_e32 v163, 0
	v_lshl_add_u64 v[140:141], v[70:71], 0, s[0:1]
	s_mov_b64 s[0:1], 0x34000a00
	v_pk_fma_f32 v[164:165], v[86:87], v[230:231], v[234:235]
	v_pk_fma_f32 v[166:167], v[88:89], v[232:233], v[236:237]
	v_bfe_u32 v168, v164, 16, 1
	v_bfe_u32 v169, v165, 16, 1
	v_pk_fma_f32 v[88:89], v[38:39], v[164:165], v[34:35]
	v_add3_u32 v164, v164, v168, s39
	v_add3_u32 v165, v165, v169, s39
	v_med3_f32 v168, v88, s40, v160
	v_med3_f32 v169, v89, s40, v160
	v_cvt_pk_fp8_f32 v163, v168, v169
	v_bfe_u32 v170, v166, 16, 1
	v_pk_fma_f32 v[86:87], v[40:41], v[166:167], v[36:37]
	v_add3_u32 v166, v166, v170, s39
	v_med3_f32 v170, v86, s40, v160
	v_med3_f32 v168, v87, s40, v160
	v_bfe_u32 v171, v167, 16, 1
	v_cvt_pk_fp8_f32 v163, v170, v168 op_sel:[0,0,1]
	v_add3_u32 v167, v167, v171, s39
	v_lshrrev_b32_e32 v164, 16, v164
	v_lshrrev_b32_e32 v166, 16, v166
	v_and_or_b32 v164, v165, s38, v164
	v_and_or_b32 v165, v167, s38, v166
	global_store_dwordx2 v[140:141], v[164:165], off
	global_store_dword v[84:85], v163, off offset:1024
	v_mov_b32_e32 v163, 0
	v_lshl_add_u64 v[140:141], v[70:71], 0, s[0:1]
	s_mov_b64 s[0:1], 0x34000c00
	v_pk_fma_f32 v[80:81], v[80:81], v[238:239], v[118:119]
	v_pk_fma_f32 v[82:83], v[82:83], v[240:241], v[120:121]
	v_bfe_u32 v164, v80, 16, 1
	v_bfe_u32 v165, v81, 16, 1
	v_pk_fma_f32 v[170:171], v[46:47], v[80:81], v[42:43]
	v_add3_u32 v80, v80, v164, s39
	v_add3_u32 v81, v81, v165, s39
	v_med3_f32 v164, v170, s40, v160
	v_med3_f32 v165, v171, s40, v160
	v_cvt_pk_fp8_f32 v163, v164, v165
	v_bfe_u32 v166, v82, 16, 1
	v_pk_fma_f32 v[168:169], v[48:49], v[82:83], v[44:45]
	v_add3_u32 v82, v82, v166, s39
	v_med3_f32 v166, v168, s40, v160
	v_med3_f32 v164, v169, s40, v160
	v_bfe_u32 v167, v83, 16, 1
	v_cvt_pk_fp8_f32 v163, v166, v164 op_sel:[0,0,1]
	v_add3_u32 v83, v83, v167, s39
	v_lshrrev_b32_e32 v80, 16, v80
	v_lshrrev_b32_e32 v82, 16, v82
	v_and_or_b32 v80, v81, s38, v80
	v_and_or_b32 v81, v83, s38, v82
	global_store_dwordx2 v[140:141], v[80:81], off
	global_store_dword v[84:85], v163, off offset:1280
	v_mov_b32_e32 v163, 0
	v_lshl_add_u64 v[140:141], v[70:71], 0, s[0:1]
	s_mov_b64 s[0:1], 0x34000e00
	v_lshl_add_u64 v[70:71], v[70:71], 0, s[0:1]
	s_mov_b64 s[0:1], 0x4000
	v_lshl_add_u64 v[66:67], v[66:67], 0, s[0:1]
	s_mov_b64 s[0:1], 0x8000
	v_lshl_add_u64 v[68:69], v[68:69], 0, s[0:1]
	v_pk_fma_f32 v[72:73], v[72:73], v[242:243], v[122:123]
	v_pk_fma_f32 v[74:75], v[74:75], v[244:245], v[124:125]
	v_bfe_u32 v76, v72, 16, 1
	v_bfe_u32 v77, v73, 16, 1
	v_pk_fma_f32 v[82:83], v[54:55], v[72:73], v[50:51]
	v_add3_u32 v72, v72, v76, s39
	v_add3_u32 v73, v73, v77, s39
	v_med3_f32 v76, v82, s40, v160
	v_med3_f32 v77, v83, s40, v160
	v_cvt_pk_fp8_f32 v163, v76, v77
	v_bfe_u32 v78, v74, 16, 1
	v_pk_fma_f32 v[80:81], v[56:57], v[74:75], v[52:53]
	v_add3_u32 v74, v74, v78, s39
	v_med3_f32 v78, v80, s40, v160
	v_med3_f32 v76, v81, s40, v160
	v_bfe_u32 v79, v75, 16, 1
	v_cvt_pk_fp8_f32 v163, v78, v76 op_sel:[0,0,1]
	v_add3_u32 v75, v75, v79, s39
	v_lshrrev_b32_e32 v72, 16, v72
	v_lshrrev_b32_e32 v74, 16, v74
	v_and_or_b32 v72, v73, s38, v72
	v_and_or_b32 v73, v75, s38, v74
	global_store_dwordx2 v[140:141], v[72:73], off
	global_store_dword v[84:85], v163, off offset:1536
	v_and_b32_sdwa v140, v101, v159 dst_sel:DWORD dst_unused:UNUSED_PAD src0_sel:WORD_1 src1_sel:DWORD
	v_add3_u32 v100, v101, v140, s39
	v_and_b32_e32 v100, 0xffff0000, v100
	v_or_b32_sdwa v98, v100, v98 dst_sel:DWORD dst_unused:UNUSED_PAD src0_sel:DWORD src1_sel:WORD_1
	ds_write2st64_b64 v113, v[92:93], v[98:99] offset1:1
	v_and_b32_sdwa v93, v105, v159 dst_sel:DWORD dst_unused:UNUSED_PAD src0_sel:WORD_1 src1_sel:DWORD
	v_and_b32_sdwa v98, v107, v159 dst_sel:DWORD dst_unused:UNUSED_PAD src0_sel:WORD_1 src1_sel:DWORD
	v_add3_u32 v93, v105, v93, s39
	v_and_b32_sdwa v92, v106, v159 dst_sel:DWORD dst_unused:UNUSED_PAD src0_sel:WORD_1 src1_sel:DWORD
	v_add3_u32 v98, v107, v98, s39
	v_and_b32_e32 v93, 0xffff0000, v93
	v_add3_u32 v92, v106, v92, s39
	v_and_b32_e32 v98, 0xffff0000, v98
	v_or_b32_sdwa v93, v93, v90 dst_sel:DWORD dst_unused:UNUSED_PAD src0_sel:DWORD src1_sel:WORD_1
	v_and_b32_sdwa v90, v94, v159 dst_sel:DWORD dst_unused:UNUSED_PAD src0_sel:WORD_1 src1_sel:DWORD
	v_and_b32_sdwa v99, v95, v159 dst_sel:DWORD dst_unused:UNUSED_PAD src0_sel:WORD_1 src1_sel:DWORD
	v_and_b32_sdwa v100, v97, v159 dst_sel:DWORD dst_unused:UNUSED_PAD src0_sel:WORD_1 src1_sel:DWORD
	v_or_b32_sdwa v92, v98, v92 dst_sel:DWORD dst_unused:UNUSED_PAD src0_sel:DWORD src1_sel:WORD_1
	v_and_b32_sdwa v98, v96, v159 dst_sel:DWORD dst_unused:UNUSED_PAD src0_sel:WORD_1 src1_sel:DWORD
	v_add3_u32 v90, v94, v90, s39
	v_add3_u32 v94, v95, v99, s39
	v_add3_u32 v95, v97, v100, s39
	v_add3_u32 v96, v96, v98, s39
	v_and_b32_e32 v94, 0xffff0000, v94
	v_and_b32_e32 v97, 0xffff0000, v95
	v_or_b32_sdwa v95, v94, v90 dst_sel:DWORD dst_unused:UNUSED_PAD src0_sel:DWORD src1_sel:WORD_1
	v_or_b32_sdwa v94, v97, v96 dst_sel:DWORD dst_unused:UNUSED_PAD src0_sel:DWORD src1_sel:WORD_1
	ds_write2st64_b64 v113, v[92:93], v[94:95] offset0:2 offset1:3
	v_and_b32_sdwa v93, v87, v159 dst_sel:DWORD dst_unused:UNUSED_PAD src0_sel:WORD_1 src1_sel:DWORD
	v_and_b32_sdwa v94, v89, v159 dst_sel:DWORD dst_unused:UNUSED_PAD src0_sel:WORD_1 src1_sel:DWORD
	v_and_b32_sdwa v90, v86, v159 dst_sel:DWORD dst_unused:UNUSED_PAD src0_sel:WORD_1 src1_sel:DWORD
	v_and_b32_sdwa v92, v88, v159 dst_sel:DWORD dst_unused:UNUSED_PAD src0_sel:WORD_1 src1_sel:DWORD
	v_add3_u32 v87, v87, v93, s39
	v_add3_u32 v89, v89, v94, s39
	v_add3_u32 v88, v88, v92, s39
	v_add3_u32 v86, v86, v90, s39
	v_and_b32_e32 v87, 0xffff0000, v87
	v_and_b32_e32 v89, 0xffff0000, v89
	v_or_b32_sdwa v87, v87, v86 dst_sel:DWORD dst_unused:UNUSED_PAD src0_sel:DWORD src1_sel:WORD_1
	v_or_b32_sdwa v86, v89, v88 dst_sel:DWORD dst_unused:UNUSED_PAD src0_sel:DWORD src1_sel:WORD_1
	v_and_b32_sdwa v89, v170, v159 dst_sel:DWORD dst_unused:UNUSED_PAD src0_sel:WORD_1 src1_sel:DWORD
	v_and_b32_sdwa v90, v169, v159 dst_sel:DWORD dst_unused:UNUSED_PAD src0_sel:WORD_1 src1_sel:DWORD
	v_and_b32_sdwa v92, v171, v159 dst_sel:DWORD dst_unused:UNUSED_PAD src0_sel:WORD_1 src1_sel:DWORD
	v_and_b32_sdwa v88, v168, v159 dst_sel:DWORD dst_unused:UNUSED_PAD src0_sel:WORD_1 src1_sel:DWORD
	v_add3_u32 v93, v170, v89, s39
	v_add3_u32 v89, v169, v90, s39
	v_add3_u32 v90, v171, v92, s39
	v_add3_u32 v88, v168, v88, s39
	v_and_b32_e32 v89, 0xffff0000, v89
	v_and_b32_e32 v90, 0xffff0000, v90
	v_or_b32_sdwa v89, v89, v88 dst_sel:DWORD dst_unused:UNUSED_PAD src0_sel:DWORD src1_sel:WORD_1
	v_or_b32_sdwa v88, v90, v93 dst_sel:DWORD dst_unused:UNUSED_PAD src0_sel:DWORD src1_sel:WORD_1
	ds_write2st64_b64 v113, v[86:87], v[88:89] offset0:4 offset1:5
	v_and_b32_sdwa v88, v81, v159 dst_sel:DWORD dst_unused:UNUSED_PAD src0_sel:WORD_1 src1_sel:DWORD
	v_and_b32_sdwa v89, v83, v159 dst_sel:DWORD dst_unused:UNUSED_PAD src0_sel:WORD_1 src1_sel:DWORD
	v_add3_u32 v81, v81, v88, s39
	v_add3_u32 v83, v83, v89, s39
	v_and_b32_sdwa v86, v80, v159 dst_sel:DWORD dst_unused:UNUSED_PAD src0_sel:WORD_1 src1_sel:DWORD
	v_and_b32_sdwa v87, v82, v159 dst_sel:DWORD dst_unused:UNUSED_PAD src0_sel:WORD_1 src1_sel:DWORD
	v_add3_u32 v82, v82, v87, s39
	v_add3_u32 v80, v80, v86, s39
	v_and_b32_e32 v81, 0xffff0000, v81
	v_and_b32_e32 v83, 0xffff0000, v83
	v_or_b32_sdwa v81, v81, v80 dst_sel:DWORD dst_unused:UNUSED_PAD src0_sel:DWORD src1_sel:WORD_1
	v_or_b32_sdwa v80, v83, v82 dst_sel:DWORD dst_unused:UNUSED_PAD src0_sel:DWORD src1_sel:WORD_1
	v_pk_fma_f32 v[72:73], v[172:173], v[250:251], v[126:127]
	v_pk_fma_f32 v[74:75], v[174:175], v[252:253], v[128:129]
	v_pk_fma_f32 v[78:79], v[58:59], v[72:73], v[62:63]
	v_bfe_u32 v82, v72, 16, 1
	v_med3_f32 v88, v78, s40, v160
	v_med3_f32 v89, v79, s40, v160
	v_cvt_pk_fp8_f32 v176, v88, v89
	v_bfe_u32 v86, v74, 16, 1
	v_bfe_u32 v87, v75, 16, 1
	v_pk_fma_f32 v[76:77], v[60:61], v[74:75], v[64:65]
	v_bfe_u32 v83, v73, 16, 1
	v_add3_u32 v72, v72, v82, s39
	v_add3_u32 v74, v74, v86, s39
	v_add3_u32 v75, v75, v87, s39
	v_and_b32_sdwa v86, v77, v159 dst_sel:DWORD dst_unused:UNUSED_PAD src0_sel:WORD_1 src1_sel:DWORD
	v_and_b32_sdwa v87, v79, v159 dst_sel:DWORD dst_unused:UNUSED_PAD src0_sel:WORD_1 src1_sel:DWORD
	v_med3_f32 v90, v76, s40, v160
	v_med3_f32 v92, v77, s40, v160
	v_add3_u32 v73, v73, v83, s39
	v_and_b32_sdwa v82, v76, v159 dst_sel:DWORD dst_unused:UNUSED_PAD src0_sel:WORD_1 src1_sel:DWORD
	v_and_b32_sdwa v83, v78, v159 dst_sel:DWORD dst_unused:UNUSED_PAD src0_sel:WORD_1 src1_sel:DWORD
	v_lshrrev_b32_e32 v72, 16, v72
	v_lshrrev_b32_e32 v74, 16, v74
	v_add3_u32 v77, v77, v86, s39
	v_add3_u32 v79, v79, v87, s39
	v_cvt_pk_fp8_f32 v176, v90, v92 op_sel:[0,0,1]
	v_add3_u32 v78, v78, v83, s39
	v_add3_u32 v76, v76, v82, s39
	v_and_or_b32 v72, v73, s38, v72
	v_and_or_b32 v73, v75, s38, v74
	v_and_b32_e32 v74, 0xffff0000, v77
	v_and_b32_e32 v75, 0xffff0000, v79
	global_store_dwordx2 v[70:71], v[72:73], off
	v_or_b32_sdwa v71, v74, v76 dst_sel:DWORD dst_unused:UNUSED_PAD src0_sel:DWORD src1_sel:WORD_1
	v_or_b32_sdwa v70, v75, v78 dst_sel:DWORD dst_unused:UNUSED_PAD src0_sel:DWORD src1_sel:WORD_1
	ds_write2st64_b64 v113, v[80:81], v[70:71] offset0:6 offset1:7
	v_add_u32_e32 v113, 0x8080, v113
	global_store_dword v[84:85], v176, off offset:1792
	s_cbranch_scc1 .LBB0_1292
	s_mov_b32 s30, s22
	s_branch .LBB0_1288

.LBB0_1296:
	v_lshl_add_u32 v73, s2, 8, v139
	ds_read2st64_b32 v[74:75], v73 offset1:48
	s_mov_b32 s0, 0xbfb8aa3b
	s_mov_b32 s22, 7
	s_waitcnt lgkmcnt(0)
	v_add_f32_e32 v74, 0, v74
	v_add_f32_e32 v76, v74, v75
	ds_read2st64_b32 v[74:75], v73 offset0:96 offset1:144
	s_waitcnt lgkmcnt(0)
	v_add_f32_e32 v74, v76, v74
	v_add_f32_e32 v76, v74, v75
	ds_read2st64_b32 v[74:75], v73 offset0:192 offset1:240
	s_waitcnt lgkmcnt(0)
	v_add_f32_e32 v74, v76, v74
	v_add_f32_e32 v74, v74, v75
	v_add_u32_e32 v75, 0x12000, v73
	ds_read_b32 v75, v75
	v_add_u32_e32 v73, 0x15000, v73
	ds_read_b32 v73, v73
	s_waitcnt lgkmcnt(1)
	v_add_f32_e32 v74, v74, v75
	s_waitcnt lgkmcnt(0)
	v_add_f32_e32 v73, v74, v73
	v_mul_f32_e32 v74, 0xbfb8aa3b, v73
	v_fma_f32 v75, v73, s0, -v74
	v_rndne_f32_e32 v76, v74
	v_fmac_f32_e32 v75, 0xb2a5705f, v73
	v_sub_f32_e32 v74, v74, v76
	v_add_f32_e32 v74, v74, v75
	v_exp_f32_e32 v74, v74
	v_cvt_i32_f32_e32 v75, v76
	s_mov_b32 s0, 0x42ce8ed0
	v_cmp_nlt_f32_e32 vcc, s0, v73
	s_mov_b32 s0, 0xc2b17218
	v_ldexp_f32 v74, v74, v75
	v_cndmask_b32_e32 v74, 0, v74, vcc
	v_cmp_ngt_f32_e32 vcc, s0, v73
	s_nop 1
	v_cndmask_b32_e32 v73, v161, v74, vcc
	v_add_f32_e32 v73, 1.0, v73
	v_div_scale_f32 v74, s[0:1], v73, v73, 1.0
	v_rcp_f32_e32 v75, v74
	s_nop 0
	v_fma_f32 v76, -v74, v75, 1.0
	v_fmac_f32_e32 v75, v76, v75
	v_div_scale_f32 v76, vcc, 1.0, v73, 1.0
	v_mul_f32_e32 v77, v76, v75
	v_fma_f32 v78, -v74, v77, v76
	v_fmac_f32_e32 v77, v78, v75
	v_fma_f32 v74, -v74, v77, v76
	v_div_fmas_f32 v74, v74, v75, v77
	v_div_fixup_f32 v73, v74, v73, 1.0
	v_add_f32_e32 v74, v115, v73
	s_waitcnt lgkmcnt(0)
	s_nop 1
	v_max_f32_dpp v75, v74, v74 quad_perm:[1,0,3,2] row_mask:0xf bank_mask:0xf
	s_waitcnt lgkmcnt(0)
	s_nop 1
	v_max_f32_dpp v75, v75, v75 quad_perm:[2,3,0,1] row_mask:0xf bank_mask:0xf
	s_waitcnt lgkmcnt(0)
	s_nop 1
	v_max_f32_dpp v75, v75, v75 row_half_mirror row_mask:0xf bank_mask:0xf
	v_cmp_eq_f32_e32 vcc, v74, v75
	s_nop 1
	v_cndmask_b32_e32 v76, 8, v142, vcc
	s_waitcnt lgkmcnt(0)
	s_nop 1
	v_min_i32_dpp v76, v76, v76 quad_perm:[1,0,3,2] row_mask:0xf bank_mask:0xf
	s_waitcnt lgkmcnt(0)
	s_nop 1
	v_min_i32_dpp v76, v76, v76 quad_perm:[2,3,0,1] row_mask:0xf bank_mask:0xf
	s_waitcnt lgkmcnt(0)
	s_nop 1
	v_min_i32_dpp v76, v76, v76 row_half_mirror row_mask:0xf bank_mask:0xf
	v_cmp_ne_u32_e32 vcc, v142, v76
	s_nop 1
	v_cndmask_b32_e32 v76, v162, v74, vcc
	s_waitcnt lgkmcnt(0)
	s_nop 1
	v_max_f32_dpp v76, v76, v76 quad_perm:[1,0,3,2] row_mask:0xf bank_mask:0xf
	s_waitcnt lgkmcnt(0)
	s_nop 1
	v_max_f32_dpp v76, v76, v76 quad_perm:[2,3,0,1] row_mask:0xf bank_mask:0xf
	s_waitcnt lgkmcnt(0)
	s_nop 1
	v_max_f32_dpp v76, v76, v76 row_half_mirror row_mask:0xf bank_mask:0xf
	v_add_f32_e32 v75, v75, v76
	s_nop 0
	v_readlane_b32 s0, v75, 0
	s_nop 1
	v_cmp_gt_f32_e32 vcc, s0, v75
	v_cmp_eq_f32_e64 s[0:1], s0, v75
	s_and_b64 s[0:1], s[6:7], s[0:1]
	s_or_b64 s[0:1], vcc, s[0:1]
	v_cndmask_b32_e64 v76, 0, 1, s[0:1]
	v_readlane_b32 s0, v75, 8
	s_nop 1
	v_cmp_gt_f32_e32 vcc, s0, v75
	v_cmp_eq_f32_e64 s[0:1], s0, v75
	s_and_b64 s[0:1], s[8:9], s[0:1]
	s_or_b64 s[0:1], vcc, s[0:1]
	v_cndmask_b32_e64 v77, 0, 1, s[0:1]
	v_readlane_b32 s0, v75, 16
	s_nop 1
	v_cmp_gt_f32_e32 vcc, s0, v75
	v_cmp_eq_f32_e64 s[0:1], s0, v75
	s_and_b64 s[0:1], s[10:11], s[0:1]
	s_or_b64 s[0:1], vcc, s[0:1]
	v_cndmask_b32_e64 v78, 0, 1, s[0:1]
	v_readlane_b32 s0, v75, 24
	s_nop 1
	v_cmp_gt_f32_e32 vcc, s0, v75
	v_cmp_eq_f32_e64 s[0:1], s0, v75
	s_and_b64 s[0:1], s[12:13], s[0:1]
	s_or_b64 s[0:1], vcc, s[0:1]
	v_cndmask_b32_e64 v79, 0, 1, s[0:1]
	v_readlane_b32 s0, v75, 32
	s_nop 1
	v_cmp_gt_f32_e32 vcc, s0, v75
	v_cmp_eq_f32_e64 s[0:1], s0, v75
	s_and_b64 s[0:1], s[14:15], s[0:1]
	s_or_b64 s[0:1], vcc, s[0:1]
	v_cndmask_b32_e64 v80, 0, 1, s[0:1]
	v_readlane_b32 s0, v75, 40
	s_nop 1
	v_cmp_gt_f32_e32 vcc, s0, v75
	v_cmp_eq_f32_e64 s[0:1], s0, v75
	s_and_b64 s[0:1], s[16:17], s[0:1]
	s_or_b64 s[0:1], vcc, s[0:1]
	v_cndmask_b32_e64 v81, 0, 1, s[0:1]
	v_readlane_b32 s0, v75, 48
	s_nop 1
	v_cmp_gt_f32_e32 vcc, s0, v75
	v_cmp_eq_f32_e64 s[0:1], s0, v75
	s_and_b64 s[0:1], s[18:19], s[0:1]
	s_or_b64 s[0:1], vcc, s[0:1]
	v_cndmask_b32_e64 v82, 0, 1, s[0:1]
	v_readlane_b32 s0, v75, 56
	s_nop 1
	v_cmp_gt_f32_e32 vcc, s0, v75
	s_nop 1
	v_cndmask_b32_e64 v75, 0, 1, vcc
	v_add_u32_e32 v75, v77, v75
	v_add3_u32 v75, v75, v76, v78
	v_add3_u32 v75, v75, v79, v80
	v_add3_u32 v75, v75, v81, v82
	v_cmp_gt_u32_e32 vcc, 4, v75
	s_nop 1
	v_cndmask_b32_e32 v75, v162, v74, vcc
	v_mov_b32_e32 v74, 0
	s_mov_b32 s22, 0

.LBB0_1330:
	v_cmp_gt_u32_e64 s[0:1], 8, v74
	s_and_b64 vcc, vcc, s[0:1]
	v_cndmask_b32_e32 v75, 0, v73, vcc
	s_waitcnt lgkmcnt(0)
	s_nop 1
	v_add_f32_dpp v75, v75, v75 quad_perm:[1,0,3,2] row_mask:0xf bank_mask:0xf
	s_waitcnt lgkmcnt(0)
	s_nop 1
	v_add_f32_dpp v75, v75, v75 quad_perm:[2,3,0,1] row_mask:0xf bank_mask:0xf
	s_waitcnt lgkmcnt(0)
	s_nop 1
	v_add_f32_dpp v75, v75, v75 row_half_mirror row_mask:0xf bank_mask:0xf
	s_waitcnt lgkmcnt(0)
	s_nop 1
	v_add_f32_dpp v75, v75, v75 row_mirror row_mask:0xf bank_mask:0xf
	ds_bpermute_b32 v76, v71, v75
	s_waitcnt lgkmcnt(0)
	v_add_f32_e32 v75, v75, v76
	ds_bpermute_b32 v76, v72, v75
	s_and_saveexec_b64 s[0:1], vcc
	s_cbranch_execz .LBB0_1332
	s_mul_i32 s22, s51, 34
	s_waitcnt lgkmcnt(0)
	v_add_f32_e32 v78, v75, v76
	s_add_i32 s22, s2, s22
	v_div_scale_f32 v79, s[28:29], v78, v78, v73
	v_lshl_or_b32 v74, s22, 3, v74
	v_rcp_f32_e32 v80, v79
	v_ashrrev_i32_e32 v75, 31, v74
	v_lshlrev_b64 v[74:75], 2, v[74:75]
	v_lshl_add_u64 v[76:77], s[24:25], 0, v[74:75]
	global_store_dword v[76:77], v1, off
	v_fma_f32 v76, -v79, v80, 1.0
	v_fmac_f32_e32 v80, v76, v80
	v_div_scale_f32 v76, vcc, v73, v78, v73
	v_mul_f32_e32 v77, v76, v80
	v_fma_f32 v81, -v79, v77, v76
	v_fmac_f32_e32 v77, v81, v80
	v_fma_f32 v76, -v79, v77, v76
	v_div_fmas_f32 v76, v76, v80, v77
	v_div_fixup_f32 v73, v76, v78, v73
	v_mul_f32_e32 v73, 0x40200000, v73
	v_lshl_add_u64 v[74:75], s[26:27], 0, v[74:75]
	v_add_u32_e32 v66, 1, v66
	global_store_dword v[74:75], v73, off

.LBB0_3036:
	s_waitcnt vmcnt(0)
	v_lshlrev_b32_e32 v92, 16, v86
	v_and_b32_e32 v93, 0xffff0000, v86
	v_lshlrev_b32_e32 v98, 16, v87
	v_and_b32_e32 v99, 0xffff0000, v87
	v_add_f32_e32 v86, v92, v93
	v_add_f32_e32 v87, v98, v99
	v_lshlrev_b32_e32 v100, 16, v84
	v_and_b32_e32 v101, 0xffff0000, v84
	v_lshlrev_b32_e32 v102, 16, v85
	v_and_b32_e32 v103, 0xffff0000, v85
	v_add_f32_e32 v86, v86, v87
	v_add_f32_e32 v84, v100, v101
	v_add_f32_e32 v85, v102, v103
	v_lshlrev_b32_e32 v104, 16, v82
	v_and_b32_e32 v105, 0xffff0000, v82
	v_lshlrev_b32_e32 v106, 16, v83
	v_and_b32_e32 v107, 0xffff0000, v83
	v_add_f32_e32 v86, 0, v86
	v_add_f32_e32 v84, v84, v85
	v_add_f32_e32 v82, v104, v105
	v_add_f32_e32 v83, v106, v107
	v_lshlrev_b32_e32 v94, 16, v80
	v_and_b32_e32 v95, 0xffff0000, v80
	v_lshlrev_b32_e32 v96, 16, v81
	v_and_b32_e32 v97, 0xffff0000, v81
	v_add_f32_e32 v84, v86, v84
	v_add_f32_e32 v82, v82, v83
	v_add_f32_e32 v80, v94, v95
	v_add_f32_e32 v81, v96, v97
	v_lshlrev_b32_e32 v86, 16, v76
	v_and_b32_e32 v87, 0xffff0000, v76
	v_lshlrev_b32_e32 v88, 16, v77
	v_and_b32_e32 v89, 0xffff0000, v77
	v_add_f32_e32 v82, v84, v82
	v_add_f32_e32 v80, v80, v81
	v_add_f32_e32 v76, v86, v87
	v_add_f32_e32 v77, v88, v89
	v_add_f32_e32 v80, v82, v80
	v_add_f32_e32 v76, v76, v77
	v_add_f32_e32 v76, v80, v76
	v_lshlrev_b32_e32 v80, 16, v72
	v_and_b32_e32 v81, 0xffff0000, v72
	v_lshlrev_b32_e32 v82, 16, v73
	v_and_b32_e32 v83, 0xffff0000, v73
	v_add_f32_e32 v72, v80, v81
	v_add_f32_e32 v73, v82, v83
	v_add_f32_e32 v72, v72, v73
	v_add_f32_e32 v76, v76, v72
	v_lshlrev_b32_e32 v72, 16, v74
	v_and_b32_e32 v73, 0xffff0000, v74
	v_lshlrev_b32_e32 v74, 16, v75
	v_and_b32_e32 v75, 0xffff0000, v75
	v_add_f32_e32 v77, v72, v73
	v_add_f32_e32 v84, v74, v75
	v_add_f32_e32 v77, v77, v84
	v_add_f32_e32 v84, v76, v77
	v_lshlrev_b32_e32 v76, 16, v78
	v_and_b32_e32 v77, 0xffff0000, v78
	v_lshlrev_b32_e32 v78, 16, v79
	v_and_b32_e32 v79, 0xffff0000, v79
	v_add_f32_e32 v85, v76, v77
	v_add_f32_e32 v90, v78, v79
	v_add_f32_e32 v85, v85, v90
	v_add_f32_e32 v84, v84, v85
	s_mov_b32 s0, 0x800000
	v_mov_b32_e32 v188, 0
	s_add_i32 s22, s30, 8
	s_cmp_gt_u32 s30, 23
	s_waitcnt lgkmcnt(0)
	s_nop 1
	v_add_f32_dpp v84, v84, v84 quad_perm:[1,0,3,2] row_mask:0xf bank_mask:0xf
	s_waitcnt lgkmcnt(0)
	s_nop 1
	v_add_f32_dpp v84, v84, v84 quad_perm:[2,3,0,1] row_mask:0xf bank_mask:0xf
	s_waitcnt lgkmcnt(0)
	s_nop 1
	v_add_f32_dpp v84, v84, v84 row_half_mirror row_mask:0xf bank_mask:0xf
	s_waitcnt lgkmcnt(0)
	s_nop 1
	v_add_f32_dpp v84, v84, v84 row_mirror row_mask:0xf bank_mask:0xf
	ds_bpermute_b32 v85, v111, v84
	s_waitcnt lgkmcnt(0)
	v_add_f32_e32 v84, v84, v85
	ds_bpermute_b32 v85, v112, v84
	s_waitcnt lgkmcnt(0)
	v_add_f32_e32 v90, v84, v85
	v_fmac_f32_e32 v93, 0xba000000, v90
	v_fmac_f32_e32 v101, 0xba000000, v90
	v_fmac_f32_e32 v99, 0xba000000, v90
	v_fmac_f32_e32 v92, 0xba000000, v90
	v_fmac_f32_e32 v103, 0xba000000, v90
	v_fmac_f32_e32 v100, 0xba000000, v90
	v_mov_b32_e32 v152, v93
	v_mov_b32_e32 v153, v101
	v_fmac_f32_e32 v98, 0xba000000, v90
	v_fmac_f32_e32 v102, 0xba000000, v90
	v_mov_b32_e32 v84, v92
	v_mov_b32_e32 v85, v100
	v_pk_mul_f32 v[152:153], v[152:153], v[152:153]
	v_mov_b32_e32 v176, v99
	v_mov_b32_e32 v177, v103
	v_pk_fma_f32 v[84:85], v[84:85], v[84:85], v[152:153]
	v_mov_b32_e32 v152, v98
	v_mov_b32_e32 v153, v102
	v_pk_mul_f32 v[176:177], v[176:177], v[176:177]
	v_fmac_f32_e32 v105, 0xba000000, v90
	v_pk_fma_f32 v[152:153], v[152:153], v[152:153], v[176:177]
	v_fmac_f32_e32 v104, 0xba000000, v90
	v_pk_add_f32 v[84:85], v[84:85], v[152:153]
	v_fmac_f32_e32 v107, 0xba000000, v90
	v_fmac_f32_e32 v106, 0xba000000, v90
	v_pk_add_f32 v[84:85], v[84:85], v[84:85] op_sel_hi:[0,1]
	v_pk_mul_f32 v[152:153], v[106:107], v[106:107]
	v_pk_mul_f32 v[176:177], v[104:105], v[104:105]
	v_fmac_f32_e32 v94, 0xba000000, v90
	v_pk_mov_b32 v[178:179], v[176:177], v[152:153] op_sel:[1,0]
	v_mov_b32_e32 v177, v153
	v_fmac_f32_e32 v95, 0xba000000, v90
	v_fmac_f32_e32 v96, 0xba000000, v90
	v_mul_f32_e32 v84, v94, v94
	v_pk_add_f32 v[152:153], v[178:179], v[176:177]
	v_fmac_f32_e32 v97, 0xba000000, v90
	v_pk_fma_f32 v[176:177], v[94:95], v[94:95], v[84:85] op_sel_hi:[1,1,0]
	v_mul_f32_e32 v84, v96, v96
	v_pk_add_f32 v[152:153], v[152:153], v[152:153] op_sel_hi:[0,1]
	v_pk_fma_f32 v[178:179], v[96:97], v[96:97], v[84:85] op_sel_hi:[1,1,0]
	v_fmac_f32_e32 v89, 0xba000000, v90
	v_fmac_f32_e32 v88, 0xba000000, v90
	v_fmac_f32_e32 v87, 0xba000000, v90
	v_fmac_f32_e32 v86, 0xba000000, v90
	v_mul_f32_e32 v176, v86, v86
	v_mul_f32_e32 v178, v87, v87
	v_mul_f32_e32 v152, v88, v88
	v_mul_f32_e32 v84, v89, v89
	v_pk_add_f32 v[176:177], v[176:177], v[178:179]
	v_pk_add_f32 v[84:85], v[152:153], v[84:85]
	v_fmac_f32_e32 v81, 0xba000000, v90
	v_pk_add_f32 v[84:85], v[176:177], v[84:85]
	v_fmac_f32_e32 v80, 0xba000000, v90
	v_fmac_f32_e32 v83, 0xba000000, v90
	v_fmac_f32_e32 v82, 0xba000000, v90
	v_pk_add_f32 v[84:85], v[84:85], v[84:85] op_sel_hi:[0,1]
	v_pk_mul_f32 v[152:153], v[82:83], v[82:83]
	v_pk_mul_f32 v[184:185], v[80:81], v[80:81]
	v_fmac_f32_e32 v72, 0xba000000, v90
	v_pk_mov_b32 v[186:187], v[184:185], v[152:153] op_sel:[1,0]
	v_mov_b32_e32 v185, v153
	v_fmac_f32_e32 v73, 0xba000000, v90
	v_fmac_f32_e32 v74, 0xba000000, v90
	v_mul_f32_e32 v84, v72, v72
	v_pk_add_f32 v[152:153], v[186:187], v[184:185]
	v_fmac_f32_e32 v75, 0xba000000, v90
	v_pk_fma_f32 v[184:185], v[72:73], v[72:73], v[84:85] op_sel_hi:[1,1,0]
	v_mul_f32_e32 v84, v74, v74
	v_pk_add_f32 v[152:153], v[152:153], v[152:153] op_sel_hi:[0,1]
	v_pk_fma_f32 v[186:187], v[74:75], v[74:75], v[84:85] op_sel_hi:[1,1,0]
	v_fmac_f32_e32 v79, 0xba000000, v90
	v_fmac_f32_e32 v78, 0xba000000, v90
	v_fmac_f32_e32 v77, 0xba000000, v90
	v_fmac_f32_e32 v76, 0xba000000, v90
	v_mul_f32_e32 v184, v76, v76
	v_mul_f32_e32 v186, v77, v77
	v_mul_f32_e32 v152, v78, v78
	v_mul_f32_e32 v84, v79, v79
	v_pk_add_f32 v[184:185], v[184:185], v[186:187]
	v_pk_add_f32 v[84:85], v[152:153], v[84:85]
	s_nop 0
	v_pk_add_f32 v[84:85], v[184:185], v[84:85]
	s_nop 0
	v_add_f32_e32 v84, v84, v85
	s_waitcnt lgkmcnt(0)
	s_nop 1
	v_add_f32_dpp v84, v84, v84 quad_perm:[1,0,3,2] row_mask:0xf bank_mask:0xf
	s_waitcnt lgkmcnt(0)
	s_nop 1
	v_add_f32_dpp v84, v84, v84 quad_perm:[2,3,0,1] row_mask:0xf bank_mask:0xf
	s_waitcnt lgkmcnt(0)
	s_nop 1
	v_add_f32_dpp v84, v84, v84 row_half_mirror row_mask:0xf bank_mask:0xf
	s_waitcnt lgkmcnt(0)
	s_nop 1
	v_add_f32_dpp v84, v84, v84 row_mirror row_mask:0xf bank_mask:0xf
	ds_bpermute_b32 v85, v111, v84
	s_waitcnt lgkmcnt(0)
	v_add_f32_e32 v84, v84, v85
	ds_bpermute_b32 v85, v112, v84
	s_waitcnt lgkmcnt(0)
	v_add_f32_e32 v84, v84, v85
	v_fmamk_f32 v84, v84, 0x3a000000, v167
	v_mul_f32_e32 v85, 0x4b800000, v84
	v_cmp_gt_f32_e32 vcc, s0, v84
	s_mov_b64 s[0:1], 0x34000000
	s_nop 0
	v_cndmask_b32_e32 v84, v84, v85, vcc
	v_rsq_f32_e32 v90, v84
	v_lshl_add_u64 v[84:85], v[70:71], 0, s[0:1]
	s_mov_b64 s[0:1], 0x34000200
	v_mul_f32_e32 v152, 0x45800000, v90
	v_cndmask_b32_e32 v90, v90, v152, vcc
	v_pk_mul_f32 v[92:93], v[92:93], v[90:91] op_sel_hi:[1,0]
	v_pk_mul_f32 v[98:99], v[98:99], v[90:91] op_sel_hi:[1,0]
	v_pk_fma_f32 v[92:93], v[208:209], v[92:93], v[242:243]
	v_pk_fma_f32 v[98:99], v[210:211], v[98:99], v[244:245]
	v_bfe_u32 v152, v92, 16, 1
	v_add3_u32 v152, v92, v152, s39
	v_bfe_u32 v153, v93, 16, 1
	v_lshrrev_b32_e32 v152, 16, v152
	v_add3_u32 v153, v93, v153, s39
	v_and_or_b32 v152, v153, s38, v152
	v_bfe_u32 v153, v98, 16, 1
	v_add3_u32 v153, v98, v153, s39
	v_bfe_u32 v175, v99, 16, 1
	v_lshrrev_b32_e32 v153, 16, v153
	v_add3_u32 v175, v99, v175, s39
	v_and_or_b32 v153, v175, s38, v153
	v_pk_fma_f32 v[92:93], v[34:35], v[92:93], v[2:3]
	global_store_dwordx2 v[84:85], v[152:153], off
	v_med3_f32 v84, v92, s40, v172
	v_med3_f32 v85, v93, s40, v172
	v_mov_b32_e32 v152, 0
	v_cvt_pk_fp8_f32 v152, v84, v85
	v_pk_fma_f32 v[98:99], v[36:37], v[98:99], v[4:5]
	v_pk_mul_f32 v[100:101], v[100:101], v[90:91] op_sel_hi:[1,0]
	v_med3_f32 v84, v98, s40, v172
	v_med3_f32 v85, v99, s40, v172
	v_cvt_pk_fp8_f32 v152, v84, v85 op_sel:[0,0,1]
	v_lshl_add_u64 v[84:85], s[92:93], 0, v[66:67]
	v_add_co_u32_e32 v84, vcc, s41, v84
	v_pk_mul_f32 v[102:103], v[102:103], v[90:91] op_sel_hi:[1,0]
	s_nop 0
	v_addc_co_u32_e32 v85, vcc, 0, v85, vcc
	global_store_dword v[84:85], v152, off
	v_lshl_add_u64 v[152:153], v[70:71], 0, s[0:1]
	v_pk_mul_f32 v[104:105], v[104:105], v[90:91] op_sel_hi:[1,0]
	v_pk_mul_f32 v[106:107], v[106:107], v[90:91] op_sel_hi:[1,0]
	s_mov_b64 s[0:1], 0x34000400
	v_pk_mul_f32 v[94:95], v[94:95], v[90:91] op_sel_hi:[1,0]
	v_pk_mul_f32 v[96:97], v[96:97], v[90:91] op_sel_hi:[1,0]
	v_pk_mul_f32 v[86:87], v[86:87], v[90:91] op_sel_hi:[1,0]
	v_pk_mul_f32 v[88:89], v[88:89], v[90:91] op_sel_hi:[1,0]
	v_pk_mul_f32 v[80:81], v[80:81], v[90:91] op_sel_hi:[1,0]
	v_pk_mul_f32 v[82:83], v[82:83], v[90:91] op_sel_hi:[1,0]
	v_pk_mul_f32 v[72:73], v[72:73], v[90:91] op_sel_hi:[1,0]
	v_pk_mul_f32 v[74:75], v[74:75], v[90:91] op_sel_hi:[1,0]
	v_pk_mul_f32 v[184:185], v[76:77], v[90:91] op_sel_hi:[1,0]
	v_and_b32_sdwa v76, v98, v171 dst_sel:DWORD dst_unused:UNUSED_PAD src0_sel:WORD_1 src1_sel:DWORD
	v_and_b32_sdwa v77, v92, v171 dst_sel:DWORD dst_unused:UNUSED_PAD src0_sel:WORD_1 src1_sel:DWORD
	v_pk_mul_f32 v[186:187], v[78:79], v[90:91] op_sel_hi:[1,0]
	v_add3_u32 v90, v92, v77, s39
	v_add3_u32 v92, v98, v76, s39
	v_and_b32_sdwa v78, v99, v171 dst_sel:DWORD dst_unused:UNUSED_PAD src0_sel:WORD_1 src1_sel:DWORD
	v_add3_u32 v98, v99, v78, s39
	v_and_b32_sdwa v79, v93, v171 dst_sel:DWORD dst_unused:UNUSED_PAD src0_sel:WORD_1 src1_sel:DWORD
	v_add3_u32 v93, v93, v79, s39
	v_and_b32_e32 v98, 0xffff0000, v98
	v_and_b32_e32 v99, 0xffff0000, v93
	v_or_b32_sdwa v93, v98, v92 dst_sel:DWORD dst_unused:UNUSED_PAD src0_sel:DWORD src1_sel:WORD_1
	v_or_b32_sdwa v92, v99, v90 dst_sel:DWORD dst_unused:UNUSED_PAD src0_sel:DWORD src1_sel:WORD_1
	v_lshl_add_u64 v[66:67], v[66:67], 0, s[48:49]
	v_pk_fma_f32 v[100:101], v[214:215], v[100:101], v[250:251]
	v_pk_fma_f32 v[178:179], v[216:217], v[102:103], v[252:253]
	v_bfe_u32 v102, v100, 16, 1
	v_add3_u32 v102, v100, v102, s39
	v_bfe_u32 v103, v101, 16, 1
	v_lshrrev_b32_e32 v102, 16, v102
	v_add3_u32 v103, v101, v103, s39
	v_and_or_b32 v176, v103, s38, v102
	v_bfe_u32 v102, v178, 16, 1
	v_add3_u32 v102, v178, v102, s39
	v_pk_fma_f32 v[100:101], v[38:39], v[100:101], v[6:7]
	v_lshrrev_b32_e32 v175, 16, v102
	v_med3_f32 v102, v100, s40, v172
	v_med3_f32 v103, v101, s40, v172
	v_mov_b32_e32 v180, 0
	v_cvt_pk_fp8_f32 v180, v102, v103
	v_pk_fma_f32 v[102:103], v[40:41], v[178:179], v[8:9]
	v_bfe_u32 v177, v179, 16, 1
	v_med3_f32 v178, v102, s40, v172
	v_med3_f32 v181, v103, s40, v172
	v_cvt_pk_fp8_f32 v180, v178, v181 op_sel:[0,0,1]
	v_add3_u32 v177, v179, v177, s39
	v_and_or_b32 v177, v177, s38, v175
	global_store_dwordx2 v[152:153], v[176:177], off
	global_store_dword v[84:85], v180, off offset:256
	v_mov_b32_e32 v175, 0
	v_lshl_add_u64 v[152:153], v[70:71], 0, s[0:1]
	s_mov_b64 s[0:1], 0x34000600
	v_and_b32_sdwa v98, v100, v171 dst_sel:DWORD dst_unused:UNUSED_PAD src0_sel:WORD_1 src1_sel:DWORD
	v_and_b32_sdwa v99, v103, v171 dst_sel:DWORD dst_unused:UNUSED_PAD src0_sel:WORD_1 src1_sel:DWORD
	v_and_b32_sdwa v90, v102, v171 dst_sel:DWORD dst_unused:UNUSED_PAD src0_sel:WORD_1 src1_sel:DWORD
	v_add3_u32 v98, v100, v98, s39
	v_add3_u32 v99, v103, v99, s39
	v_add3_u32 v90, v102, v90, s39
	v_and_b32_e32 v99, 0xffff0000, v99
	v_or_b32_sdwa v99, v99, v90 dst_sel:DWORD dst_unused:UNUSED_PAD src0_sel:DWORD src1_sel:WORD_1
	v_pk_fma_f32 v[176:177], v[218:219], v[104:105], v[118:119]
	v_pk_fma_f32 v[178:179], v[220:221], v[106:107], v[120:121]
	v_bfe_u32 v180, v176, 16, 1
	v_bfe_u32 v181, v177, 16, 1
; #define GAS __attribute__((address_space(1)))
; #define LAS __attribute__((address_space(3)))
; __device__ __forceinline__ unsigned pk2(float lo, float hi) { return f2bf(lo) | (f2bf(hi) << 16); }
; __device__ __forceinline__ unsigned pk4_fp8(float a, float b, float c, float d) { int w = 0; w = __builtin_amdgcn_cvt_pk_fp8_f32(sat8(a), sat8(b), w, false); w = __builtin_amdgcn_cvt_pk_fp8_f32(sat8(c), sat8(d), w, true); return (unsigned)w; }
; __device__ __forceinline__ const float* modp(const unsigned char* ws, int layer, int r, int chunk) { return (const float*)(ws + WS_MOD) + ((size_t)(layer * 3 + r) * 6 + chunk) * D; }
; __device__ __forceinline__ void phase_ln_router(const Frame& F, const Args& a, int layer) {
;     ...
;         for (int j = F.wave; j < TPB; j += 8) { const int row = rb + j; bf16_t* xr = X + (size_t)row * D;
;             f32x4 v[8]; float s = 0.f;
; #pragma unroll
;             for (int i = 0; i < 8; ++i) { const u32x2 p = *(const GAS u32x2*)(xr + 4 * F.lane + 256 * i); v[i] = (f32x4){bflo(p.x), bfhi(p.x), bflo(p.y), bfhi(p.y)}; s += (v[i][0] + v[i][1]) + (v[i][2] + v[i][3]); }
;             const int r = modrow(row);
;             if (r != rcur) { rcur = r; const float* sh2 = modp(F.ws, layer, r, 3); const float* sc2 = modp(F.ws, layer, r, 4);
; #pragma unroll
;                 for (int i = 0; i < 8; ++i) { const int c = 4 * F.lane + 256 * i; psc[i] = *(const GAS f32x4*)(sc2 + c) + 1.0f; psh[i] = *(const GAS f32x4*)(sh2 + c); } }
;             const float mean = wave_sum(s) * (1.0f / D); float ss = 0.f;
; #pragma unroll
;             for (int i = 0; i < 8; ++i) { v[i] = v[i] - mean; ss += (v[i][0] * v[i][0] + v[i][1] * v[i][1]) + (v[i][2] * v[i][2] + v[i][3] * v[i][3]); }
;             const float rstd = rsqrtf(wave_sum(ss) * (1.0f / D) + LN_EPS);
; #pragma unroll
;             for (int i = 0; i < 8; ++i) { const int c = 4 * F.lane + 256 * i;
;                 const f32x4 lat = v[i] * rstd * *(const GAS f32x4*)(lng + c) + *(const GAS f32x4*)(lnb + c);
;                 { u32x2 wl; wl.x = pk2(lat[0], lat[1]); wl.y = pk2(lat[2], lat[3]); *(GAS u32x2*)(xr + c) = wl; }
;                 const f32x4 h = lat * psc[i] + psh[i];
;                 u32x2 w; w.x = pk2(h[0], h[1]); w.y = pk2(h[2], h[3]); *(GAS unsigned*)((unsigned char*)A0 + (size_t)row * D + c) = pk4_fp8(h[0], h[1], h[2], h[3]);
;                 *(LAS u32x2*)(hb + j * HB_LD + c) = w; } }
	v_pk_fma_f32 v[106:107], v[42:43], v[176:177], v[10:11]
	v_add3_u32 v176, v176, v180, s39
	v_add3_u32 v177, v177, v181, s39
	v_med3_f32 v180, v106, s40, v172
	v_med3_f32 v181, v107, s40, v172
	v_cvt_pk_fp8_f32 v175, v180, v181
	v_bfe_u32 v182, v178, 16, 1
	v_pk_fma_f32 v[104:105], v[44:45], v[178:179], v[12:13]
	v_add3_u32 v178, v178, v182, s39
	v_med3_f32 v182, v104, s40, v172
	v_med3_f32 v180, v105, s40, v172
	v_bfe_u32 v183, v179, 16, 1
	v_cvt_pk_fp8_f32 v175, v182, v180 op_sel:[0,0,1]
	v_add3_u32 v179, v179, v183, s39
	v_lshrrev_b32_e32 v176, 16, v176
	v_lshrrev_b32_e32 v178, 16, v178
	v_and_or_b32 v176, v177, s38, v176
	v_and_or_b32 v177, v179, s38, v178
	global_store_dwordx2 v[152:153], v[176:177], off
	global_store_dword v[84:85], v175, off offset:512
	v_mov_b32_e32 v175, 0
	v_lshl_add_u64 v[152:153], v[70:71], 0, s[0:1]
	s_mov_b64 s[0:1], 0x34000800
	v_and_b32_sdwa v90, v104, v171 dst_sel:DWORD dst_unused:UNUSED_PAD src0_sel:WORD_1 src1_sel:DWORD
	v_add3_u32 v90, v104, v90, s39
	v_pk_fma_f32 v[176:177], v[222:223], v[94:95], v[122:123]
	v_pk_fma_f32 v[178:179], v[224:225], v[96:97], v[124:125]
	v_bfe_u32 v180, v176, 16, 1
	v_bfe_u32 v181, v177, 16, 1
	v_pk_fma_f32 v[96:97], v[46:47], v[176:177], v[14:15]
	v_add3_u32 v176, v176, v180, s39
	v_add3_u32 v177, v177, v181, s39
	v_med3_f32 v180, v96, s40, v172
	v_med3_f32 v181, v97, s40, v172
	v_cvt_pk_fp8_f32 v175, v180, v181
	v_bfe_u32 v182, v178, 16, 1
	v_pk_fma_f32 v[94:95], v[48:49], v[178:179], v[16:17]
	v_add3_u32 v178, v178, v182, s39
	v_med3_f32 v182, v94, s40, v172
	v_med3_f32 v180, v95, s40, v172
	v_bfe_u32 v183, v179, 16, 1
	v_cvt_pk_fp8_f32 v175, v182, v180 op_sel:[0,0,1]
	v_add3_u32 v179, v179, v183, s39
	v_lshrrev_b32_e32 v176, 16, v176
	v_lshrrev_b32_e32 v178, 16, v178
	v_and_or_b32 v176, v177, s38, v176
	v_and_or_b32 v177, v179, s38, v178
	global_store_dwordx2 v[152:153], v[176:177], off
	global_store_dword v[84:85], v175, off offset:768
	v_mov_b32_e32 v175, 0
	v_lshl_add_u64 v[152:153], v[70:71], 0, s[0:1]
	s_mov_b64 s[0:1], 0x34000a00
	v_pk_fma_f32 v[176:177], v[86:87], v[226:227], v[126:127]
	v_pk_fma_f32 v[178:179], v[88:89], v[228:229], v[128:129]
	v_bfe_u32 v180, v176, 16, 1
	v_bfe_u32 v181, v177, 16, 1
	v_pk_fma_f32 v[88:89], v[50:51], v[176:177], v[18:19]
	v_add3_u32 v176, v176, v180, s39
	v_add3_u32 v177, v177, v181, s39
	v_med3_f32 v180, v88, s40, v172
	v_med3_f32 v181, v89, s40, v172
	v_cvt_pk_fp8_f32 v175, v180, v181
	v_bfe_u32 v182, v178, 16, 1
	v_pk_fma_f32 v[86:87], v[52:53], v[178:179], v[20:21]
	v_add3_u32 v178, v178, v182, s39
	v_med3_f32 v182, v86, s40, v172
	v_med3_f32 v180, v87, s40, v172
	v_bfe_u32 v183, v179, 16, 1
	v_cvt_pk_fp8_f32 v175, v182, v180 op_sel:[0,0,1]
	v_add3_u32 v179, v179, v183, s39
	v_lshrrev_b32_e32 v176, 16, v176
	v_lshrrev_b32_e32 v178, 16, v178
	v_and_or_b32 v176, v177, s38, v176
	v_and_or_b32 v177, v179, s38, v178
	global_store_dwordx2 v[152:153], v[176:177], off
	global_store_dword v[84:85], v175, off offset:1024
	v_mov_b32_e32 v175, 0
	v_lshl_add_u64 v[152:153], v[70:71], 0, s[0:1]
	s_mov_b64 s[0:1], 0x34000c00
	v_pk_fma_f32 v[80:81], v[80:81], v[230:231], v[130:131]
	v_pk_fma_f32 v[82:83], v[82:83], v[232:233], v[132:133]
	v_bfe_u32 v176, v80, 16, 1
	v_bfe_u32 v177, v81, 16, 1
	v_pk_fma_f32 v[182:183], v[54:55], v[80:81], v[22:23]
	v_add3_u32 v80, v80, v176, s39
	v_add3_u32 v81, v81, v177, s39
	v_med3_f32 v176, v182, s40, v172
	v_med3_f32 v177, v183, s40, v172
	v_cvt_pk_fp8_f32 v175, v176, v177
	v_bfe_u32 v178, v82, 16, 1
	v_pk_fma_f32 v[180:181], v[56:57], v[82:83], v[24:25]
	v_add3_u32 v82, v82, v178, s39
	v_med3_f32 v178, v180, s40, v172
	v_med3_f32 v176, v181, s40, v172
	v_bfe_u32 v179, v83, 16, 1
	v_cvt_pk_fp8_f32 v175, v178, v176 op_sel:[0,0,1]
	v_add3_u32 v83, v83, v179, s39
	v_lshrrev_b32_e32 v80, 16, v80
	v_lshrrev_b32_e32 v82, 16, v82
	v_and_or_b32 v80, v81, s38, v80
	v_and_or_b32 v81, v83, s38, v82
	global_store_dwordx2 v[152:153], v[80:81], off
	global_store_dword v[84:85], v175, off offset:1280
	v_mov_b32_e32 v175, 0
	v_lshl_add_u64 v[152:153], v[70:71], 0, s[0:1]
	s_mov_b64 s[0:1], 0x34000e00
	v_lshl_add_u64 v[70:71], v[70:71], 0, s[0:1]
	s_mov_b64 s[0:1], 0x8000
	v_lshl_add_u64 v[68:69], v[68:69], 0, s[0:1]
	v_pk_fma_f32 v[72:73], v[72:73], v[234:235], v[134:135]
	v_pk_fma_f32 v[74:75], v[74:75], v[236:237], v[136:137]
	v_bfe_u32 v76, v72, 16, 1
	v_bfe_u32 v77, v73, 16, 1
	v_pk_fma_f32 v[82:83], v[58:59], v[72:73], v[26:27]
	v_add3_u32 v72, v72, v76, s39
	v_add3_u32 v73, v73, v77, s39
	v_med3_f32 v76, v82, s40, v172
	v_med3_f32 v77, v83, s40, v172
	v_cvt_pk_fp8_f32 v175, v76, v77
	v_bfe_u32 v78, v74, 16, 1
	v_pk_fma_f32 v[80:81], v[60:61], v[74:75], v[28:29]
	v_add3_u32 v74, v74, v78, s39
	v_med3_f32 v78, v80, s40, v172
	v_med3_f32 v76, v81, s40, v172
	v_bfe_u32 v79, v75, 16, 1
	v_cvt_pk_fp8_f32 v175, v78, v76 op_sel:[0,0,1]
	v_add3_u32 v75, v75, v79, s39
	v_lshrrev_b32_e32 v72, 16, v72
	v_lshrrev_b32_e32 v74, 16, v74
	v_and_or_b32 v72, v73, s38, v72
	v_and_or_b32 v73, v75, s38, v74
	global_store_dwordx2 v[152:153], v[72:73], off
	global_store_dword v[84:85], v175, off offset:1536
	v_and_b32_sdwa v152, v101, v171 dst_sel:DWORD dst_unused:UNUSED_PAD src0_sel:WORD_1 src1_sel:DWORD
	v_add3_u32 v100, v101, v152, s39
	v_and_b32_e32 v100, 0xffff0000, v100
	v_or_b32_sdwa v98, v100, v98 dst_sel:DWORD dst_unused:UNUSED_PAD src0_sel:DWORD src1_sel:WORD_1
	ds_write2st64_b64 v113, v[92:93], v[98:99] offset1:1
	v_and_b32_sdwa v93, v105, v171 dst_sel:DWORD dst_unused:UNUSED_PAD src0_sel:WORD_1 src1_sel:DWORD
	v_and_b32_sdwa v98, v107, v171 dst_sel:DWORD dst_unused:UNUSED_PAD src0_sel:WORD_1 src1_sel:DWORD
; #define GAS __attribute__((address_space(1)))
; #define LAS __attribute__((address_space(3)))
; __device__ __forceinline__ unsigned pk2(float lo, float hi) { return f2bf(lo) | (f2bf(hi) << 16); }
; __device__ __forceinline__ unsigned pk4_fp8(float a, float b, float c, float d) { int w = 0; w = __builtin_amdgcn_cvt_pk_fp8_f32(sat8(a), sat8(b), w, false); w = __builtin_amdgcn_cvt_pk_fp8_f32(sat8(c), sat8(d), w, true); return (unsigned)w; }
; __device__ __forceinline__ const float* modp(const unsigned char* ws, int layer, int r, int chunk) { return (const float*)(ws + WS_MOD) + ((size_t)(layer * 3 + r) * 6 + chunk) * D; }
; __device__ __forceinline__ void phase_ln_router(const Frame& F, const Args& a, int layer) {
;     ...
;         for (int j = F.wave; j < TPB; j += 8) { const int row = rb + j; bf16_t* xr = X + (size_t)row * D;
;             f32x4 v[8]; float s = 0.f;
; #pragma unroll
;             for (int i = 0; i < 8; ++i) { const u32x2 p = *(const GAS u32x2*)(xr + 4 * F.lane + 256 * i); v[i] = (f32x4){bflo(p.x), bfhi(p.x), bflo(p.y), bfhi(p.y)}; s += (v[i][0] + v[i][1]) + (v[i][2] + v[i][3]); }
;             const int r = modrow(row);
;             if (r != rcur) { rcur = r; const float* sh2 = modp(F.ws, layer, r, 3); const float* sc2 = modp(F.ws, layer, r, 4);
; #pragma unroll
;                 for (int i = 0; i < 8; ++i) { const int c = 4 * F.lane + 256 * i; psc[i] = *(const GAS f32x4*)(sc2 + c) + 1.0f; psh[i] = *(const GAS f32x4*)(sh2 + c); } }
;             const float mean = wave_sum(s) * (1.0f / D); float ss = 0.f;
; #pragma unroll
;             for (int i = 0; i < 8; ++i) { v[i] = v[i] - mean; ss += (v[i][0] * v[i][0] + v[i][1] * v[i][1]) + (v[i][2] * v[i][2] + v[i][3] * v[i][3]); }
;             const float rstd = rsqrtf(wave_sum(ss) * (1.0f / D) + LN_EPS);
; #pragma unroll
;             for (int i = 0; i < 8; ++i) { const int c = 4 * F.lane + 256 * i;
;                 const f32x4 lat = v[i] * rstd * *(const GAS f32x4*)(lng + c) + *(const GAS f32x4*)(lnb + c);
;                 { u32x2 wl; wl.x = pk2(lat[0], lat[1]); wl.y = pk2(lat[2], lat[3]); *(GAS u32x2*)(xr + c) = wl; }
;                 const f32x4 h = lat * psc[i] + psh[i];
;                 u32x2 w; w.x = pk2(h[0], h[1]); w.y = pk2(h[2], h[3]); *(GAS unsigned*)((unsigned char*)A0 + (size_t)row * D + c) = pk4_fp8(h[0], h[1], h[2], h[3]);
;                 *(LAS u32x2*)(hb + j * HB_LD + c) = w; } }
	v_add3_u32 v93, v105, v93, s39
	v_and_b32_sdwa v92, v106, v171 dst_sel:DWORD dst_unused:UNUSED_PAD src0_sel:WORD_1 src1_sel:DWORD
	v_add3_u32 v98, v107, v98, s39
	v_and_b32_e32 v93, 0xffff0000, v93
	v_add3_u32 v92, v106, v92, s39
	v_and_b32_e32 v98, 0xffff0000, v98
	v_or_b32_sdwa v93, v93, v90 dst_sel:DWORD dst_unused:UNUSED_PAD src0_sel:DWORD src1_sel:WORD_1
	v_and_b32_sdwa v90, v94, v171 dst_sel:DWORD dst_unused:UNUSED_PAD src0_sel:WORD_1 src1_sel:DWORD
	v_and_b32_sdwa v99, v95, v171 dst_sel:DWORD dst_unused:UNUSED_PAD src0_sel:WORD_1 src1_sel:DWORD
	v_and_b32_sdwa v100, v97, v171 dst_sel:DWORD dst_unused:UNUSED_PAD src0_sel:WORD_1 src1_sel:DWORD
	v_or_b32_sdwa v92, v98, v92 dst_sel:DWORD dst_unused:UNUSED_PAD src0_sel:DWORD src1_sel:WORD_1
	v_and_b32_sdwa v98, v96, v171 dst_sel:DWORD dst_unused:UNUSED_PAD src0_sel:WORD_1 src1_sel:DWORD
	v_add3_u32 v90, v94, v90, s39
	v_add3_u32 v94, v95, v99, s39
	v_add3_u32 v95, v97, v100, s39
	v_add3_u32 v96, v96, v98, s39
	v_and_b32_e32 v94, 0xffff0000, v94
	v_and_b32_e32 v97, 0xffff0000, v95
	v_or_b32_sdwa v95, v94, v90 dst_sel:DWORD dst_unused:UNUSED_PAD src0_sel:DWORD src1_sel:WORD_1
	v_or_b32_sdwa v94, v97, v96 dst_sel:DWORD dst_unused:UNUSED_PAD src0_sel:DWORD src1_sel:WORD_1
	ds_write2st64_b64 v113, v[92:93], v[94:95] offset0:2 offset1:3
	v_and_b32_sdwa v93, v87, v171 dst_sel:DWORD dst_unused:UNUSED_PAD src0_sel:WORD_1 src1_sel:DWORD
	v_and_b32_sdwa v94, v89, v171 dst_sel:DWORD dst_unused:UNUSED_PAD src0_sel:WORD_1 src1_sel:DWORD
	v_and_b32_sdwa v90, v86, v171 dst_sel:DWORD dst_unused:UNUSED_PAD src0_sel:WORD_1 src1_sel:DWORD
	v_and_b32_sdwa v92, v88, v171 dst_sel:DWORD dst_unused:UNUSED_PAD src0_sel:WORD_1 src1_sel:DWORD
	v_add3_u32 v87, v87, v93, s39
	v_add3_u32 v89, v89, v94, s39
	v_add3_u32 v88, v88, v92, s39
	v_add3_u32 v86, v86, v90, s39
	v_and_b32_e32 v87, 0xffff0000, v87
	v_and_b32_e32 v89, 0xffff0000, v89
	v_or_b32_sdwa v87, v87, v86 dst_sel:DWORD dst_unused:UNUSED_PAD src0_sel:DWORD src1_sel:WORD_1
	v_or_b32_sdwa v86, v89, v88 dst_sel:DWORD dst_unused:UNUSED_PAD src0_sel:DWORD src1_sel:WORD_1
	v_and_b32_sdwa v89, v182, v171 dst_sel:DWORD dst_unused:UNUSED_PAD src0_sel:WORD_1 src1_sel:DWORD
	v_and_b32_sdwa v90, v181, v171 dst_sel:DWORD dst_unused:UNUSED_PAD src0_sel:WORD_1 src1_sel:DWORD
	v_and_b32_sdwa v92, v183, v171 dst_sel:DWORD dst_unused:UNUSED_PAD src0_sel:WORD_1 src1_sel:DWORD
	v_and_b32_sdwa v88, v180, v171 dst_sel:DWORD dst_unused:UNUSED_PAD src0_sel:WORD_1 src1_sel:DWORD
	v_add3_u32 v93, v182, v89, s39
	v_add3_u32 v89, v181, v90, s39
	v_add3_u32 v90, v183, v92, s39
	v_add3_u32 v88, v180, v88, s39
	v_and_b32_e32 v89, 0xffff0000, v89
	v_and_b32_e32 v90, 0xffff0000, v90
	v_or_b32_sdwa v89, v89, v88 dst_sel:DWORD dst_unused:UNUSED_PAD src0_sel:DWORD src1_sel:WORD_1
	v_or_b32_sdwa v88, v90, v93 dst_sel:DWORD dst_unused:UNUSED_PAD src0_sel:DWORD src1_sel:WORD_1
	ds_write2st64_b64 v113, v[86:87], v[88:89] offset0:4 offset1:5
	v_and_b32_sdwa v88, v81, v171 dst_sel:DWORD dst_unused:UNUSED_PAD src0_sel:WORD_1 src1_sel:DWORD
	v_and_b32_sdwa v89, v83, v171 dst_sel:DWORD dst_unused:UNUSED_PAD src0_sel:WORD_1 src1_sel:DWORD
	v_add3_u32 v81, v81, v88, s39
	v_add3_u32 v83, v83, v89, s39
	v_and_b32_sdwa v86, v80, v171 dst_sel:DWORD dst_unused:UNUSED_PAD src0_sel:WORD_1 src1_sel:DWORD
	v_and_b32_sdwa v87, v82, v171 dst_sel:DWORD dst_unused:UNUSED_PAD src0_sel:WORD_1 src1_sel:DWORD
	v_add3_u32 v82, v82, v87, s39
	v_add3_u32 v80, v80, v86, s39
	v_and_b32_e32 v81, 0xffff0000, v81
	v_and_b32_e32 v83, 0xffff0000, v83
	v_or_b32_sdwa v81, v81, v80 dst_sel:DWORD dst_unused:UNUSED_PAD src0_sel:DWORD src1_sel:WORD_1
	v_or_b32_sdwa v80, v83, v82 dst_sel:DWORD dst_unused:UNUSED_PAD src0_sel:DWORD src1_sel:WORD_1
	v_pk_fma_f32 v[72:73], v[184:185], v[238:239], v[138:139]
	v_pk_fma_f32 v[74:75], v[186:187], v[240:241], v[140:141]
	v_pk_fma_f32 v[78:79], v[62:63], v[72:73], v[30:31]
	v_bfe_u32 v82, v72, 16, 1
	v_med3_f32 v88, v78, s40, v172
	v_med3_f32 v89, v79, s40, v172
	v_cvt_pk_fp8_f32 v188, v88, v89
	v_bfe_u32 v86, v74, 16, 1
	v_bfe_u32 v87, v75, 16, 1
	v_pk_fma_f32 v[76:77], v[64:65], v[74:75], v[32:33]
	v_bfe_u32 v83, v73, 16, 1
	v_add3_u32 v72, v72, v82, s39
	v_add3_u32 v74, v74, v86, s39
	v_add3_u32 v75, v75, v87, s39
	v_and_b32_sdwa v86, v77, v171 dst_sel:DWORD dst_unused:UNUSED_PAD src0_sel:WORD_1 src1_sel:DWORD
	v_and_b32_sdwa v87, v79, v171 dst_sel:DWORD dst_unused:UNUSED_PAD src0_sel:WORD_1 src1_sel:DWORD
	v_med3_f32 v90, v76, s40, v172
	v_med3_f32 v92, v77, s40, v172
	v_add3_u32 v73, v73, v83, s39
	v_and_b32_sdwa v82, v76, v171 dst_sel:DWORD dst_unused:UNUSED_PAD src0_sel:WORD_1 src1_sel:DWORD
	v_and_b32_sdwa v83, v78, v171 dst_sel:DWORD dst_unused:UNUSED_PAD src0_sel:WORD_1 src1_sel:DWORD
	v_lshrrev_b32_e32 v72, 16, v72
	v_lshrrev_b32_e32 v74, 16, v74
	v_add3_u32 v77, v77, v86, s39
	v_add3_u32 v79, v79, v87, s39
	v_cvt_pk_fp8_f32 v188, v90, v92 op_sel:[0,0,1]
	v_add3_u32 v78, v78, v83, s39
	v_add3_u32 v76, v76, v82, s39
	v_and_or_b32 v72, v73, s38, v72
	v_and_or_b32 v73, v75, s38, v74
	v_and_b32_e32 v74, 0xffff0000, v77
	v_and_b32_e32 v75, 0xffff0000, v79
	global_store_dwordx2 v[70:71], v[72:73], off
	v_or_b32_sdwa v71, v74, v76 dst_sel:DWORD dst_unused:UNUSED_PAD src0_sel:DWORD src1_sel:WORD_1
	v_or_b32_sdwa v70, v75, v78 dst_sel:DWORD dst_unused:UNUSED_PAD src0_sel:DWORD src1_sel:WORD_1
	ds_write2st64_b64 v113, v[80:81], v[70:71] offset0:6 offset1:7
	v_add_u32_e32 v113, 0x8080, v113
	global_store_dword v[84:85], v188, off offset:1792
	s_cbranch_scc1 .LBB0_3038
	s_mov_b32 s30, s22
	s_branch .LBB0_3034

; __device__ __forceinline__ void phase_ln_router(const Frame& F, const Args& a, int layer) {
;     ...
;         for (int j = F.wave; j < TPB; j += 8) { const int row = rb + j; float logit = 0.f;
; #pragma unroll
;             for (int w = 0; w < 8; ++w) logit += part[(w * 48 + j) * 64 + F.lane];
;             const float sg = 1.0f / (1.0f + expf(-logit)), bsd = sg + rbias;
;             float m1 = bsd;
; #pragma unroll
;             for (int o = 1; o < 8; o <<= 1) m1 = fmaxf(m1, __shfl_xor(m1, o));
;             int idx = (bsd == m1) ? (F.lane & 7) : 8;
; #pragma unroll
;             for (int o = 1; o < 8; o <<= 1) idx = min(idx, __shfl_xor(idx, o));
;             float m2 = ((F.lane & 7) == idx) ? -INFINITY : bsd;
; #pragma unroll
;             for (int o = 1; o < 8; o <<= 1) m2 = fmaxf(m2, __shfl_xor(m2, o));
;             const float gs = m1 + m2; const int mygrp = F.lane >> 3; int grank = 0;
; #pragma unroll
;             for (int gg = 0; gg < 8; ++gg) { const float og = __builtin_bit_cast(float, __builtin_amdgcn_readlane(__builtin_bit_cast(int, gs), gg * 8)); grank += (og > gs || (og == gs && gg < mygrp)) ? 1 : 0; }
;             const bool gsel = grank < 4; const float cand = gsel ? bsd : -INFINITY; int rank = 0;
.LBB0_3042:
	v_lshl_add_u32 v73, s22, 8, v151
	ds_read2st64_b32 v[74:75], v73 offset1:48
	s_mov_b32 s33, 7
	s_waitcnt lgkmcnt(0)
	v_add_f32_e32 v74, 0, v74
	v_add_f32_e32 v76, v74, v75
	ds_read2st64_b32 v[74:75], v73 offset0:96 offset1:144
	s_waitcnt lgkmcnt(0)
	v_add_f32_e32 v74, v76, v74
	v_add_f32_e32 v76, v74, v75
	ds_read2st64_b32 v[74:75], v73 offset0:192 offset1:240
	s_waitcnt lgkmcnt(0)
	v_add_f32_e32 v74, v76, v74
	v_add_f32_e32 v74, v74, v75
	v_add_u32_e32 v75, 0x12000, v73
	ds_read_b32 v75, v75
	v_add_u32_e32 v73, 0x15000, v73
	ds_read_b32 v73, v73
	s_waitcnt lgkmcnt(1)
	v_add_f32_e32 v74, v74, v75
	s_waitcnt lgkmcnt(0)
	v_add_f32_e32 v73, v74, v73
	v_mul_f32_e32 v74, 0xbfb8aa3b, v73
	v_fma_f32 v75, v73, s54, -v74
	v_rndne_f32_e32 v76, v74
	v_fmac_f32_e32 v75, 0xb2a5705f, v73
	v_sub_f32_e32 v74, v74, v76
	v_add_f32_e32 v74, v74, v75
	v_exp_f32_e32 v74, v74
	v_cvt_i32_f32_e32 v75, v76
	v_cmp_nlt_f32_e32 vcc, s55, v73
	v_ldexp_f32 v74, v74, v75
	s_nop 0
	v_cndmask_b32_e32 v74, 0, v74, vcc
	v_cmp_ngt_f32_e32 vcc, s56, v73
	s_nop 1
	v_cndmask_b32_e32 v73, v173, v74, vcc
	v_add_f32_e32 v73, 1.0, v73
	v_div_scale_f32 v74, s[0:1], v73, v73, 1.0
	v_rcp_f32_e32 v75, v74
	s_nop 0
	v_fma_f32 v76, -v74, v75, 1.0
	v_fmac_f32_e32 v75, v76, v75
	v_div_scale_f32 v76, vcc, 1.0, v73, 1.0
	v_mul_f32_e32 v77, v76, v75
	v_fma_f32 v78, -v74, v77, v76
	v_fmac_f32_e32 v77, v78, v75
	v_fma_f32 v74, -v74, v77, v76
	v_div_fmas_f32 v74, v74, v75, v77
	v_div_fixup_f32 v73, v74, v73, 1.0
	v_add_f32_e32 v74, v115, v73
	s_waitcnt lgkmcnt(0)
	s_nop 1
	v_max_f32_dpp v75, v74, v74 quad_perm:[1,0,3,2] row_mask:0xf bank_mask:0xf
	s_waitcnt lgkmcnt(0)
	s_nop 1
	v_max_f32_dpp v75, v75, v75 quad_perm:[2,3,0,1] row_mask:0xf bank_mask:0xf
	s_waitcnt lgkmcnt(0)
	s_nop 1
	v_max_f32_dpp v75, v75, v75 row_half_mirror row_mask:0xf bank_mask:0xf
	v_cmp_eq_f32_e32 vcc, v74, v75
	s_nop 1
	v_cndmask_b32_e32 v76, 8, v154, vcc
	s_waitcnt lgkmcnt(0)
	s_nop 1
	v_min_i32_dpp v76, v76, v76 quad_perm:[1,0,3,2] row_mask:0xf bank_mask:0xf
	s_waitcnt lgkmcnt(0)
	s_nop 1
	v_min_i32_dpp v76, v76, v76 quad_perm:[2,3,0,1] row_mask:0xf bank_mask:0xf
	s_waitcnt lgkmcnt(0)
	s_nop 1
	v_min_i32_dpp v76, v76, v76 row_half_mirror row_mask:0xf bank_mask:0xf
	v_cmp_ne_u32_e32 vcc, v154, v76
	s_nop 1
	v_cndmask_b32_e32 v76, v174, v74, vcc
	s_waitcnt lgkmcnt(0)
	s_nop 1
	v_max_f32_dpp v76, v76, v76 quad_perm:[1,0,3,2] row_mask:0xf bank_mask:0xf
	s_waitcnt lgkmcnt(0)
	s_nop 1
	v_max_f32_dpp v76, v76, v76 quad_perm:[2,3,0,1] row_mask:0xf bank_mask:0xf
	s_waitcnt lgkmcnt(0)
	s_nop 1
	v_max_f32_dpp v76, v76, v76 row_half_mirror row_mask:0xf bank_mask:0xf
	v_add_f32_e32 v75, v75, v76
	s_nop 0
	v_readlane_b32 s0, v75, 0
	s_nop 1
	v_cmp_gt_f32_e32 vcc, s0, v75
	v_cmp_eq_f32_e64 s[0:1], s0, v75
	s_and_b64 s[0:1], s[6:7], s[0:1]
	s_or_b64 s[0:1], vcc, s[0:1]
	v_cndmask_b32_e64 v76, 0, 1, s[0:1]
	v_readlane_b32 s0, v75, 8
	s_nop 1
	v_cmp_gt_f32_e32 vcc, s0, v75
	v_cmp_eq_f32_e64 s[0:1], s0, v75
	s_and_b64 s[0:1], s[8:9], s[0:1]
	s_or_b64 s[0:1], vcc, s[0:1]
	v_cndmask_b32_e64 v77, 0, 1, s[0:1]
	v_readlane_b32 s0, v75, 16
	s_nop 1
	v_cmp_gt_f32_e32 vcc, s0, v75
	v_cmp_eq_f32_e64 s[0:1], s0, v75
	s_and_b64 s[0:1], s[10:11], s[0:1]
	s_or_b64 s[0:1], vcc, s[0:1]
	v_cndmask_b32_e64 v78, 0, 1, s[0:1]
	v_readlane_b32 s0, v75, 24
	s_nop 1
	v_cmp_gt_f32_e32 vcc, s0, v75
	v_cmp_eq_f32_e64 s[0:1], s0, v75
	s_and_b64 s[0:1], s[12:13], s[0:1]
	s_or_b64 s[0:1], vcc, s[0:1]
	v_cndmask_b32_e64 v79, 0, 1, s[0:1]
	v_readlane_b32 s0, v75, 32
	s_nop 1
	v_cmp_gt_f32_e32 vcc, s0, v75
	v_cmp_eq_f32_e64 s[0:1], s0, v75
	s_and_b64 s[0:1], s[14:15], s[0:1]
	s_or_b64 s[0:1], vcc, s[0:1]
	v_cndmask_b32_e64 v80, 0, 1, s[0:1]
	v_readlane_b32 s0, v75, 40
	s_nop 1
	v_cmp_gt_f32_e32 vcc, s0, v75
	v_cmp_eq_f32_e64 s[0:1], s0, v75
	s_and_b64 s[0:1], s[16:17], s[0:1]
	s_or_b64 s[0:1], vcc, s[0:1]
	v_cndmask_b32_e64 v81, 0, 1, s[0:1]
	v_readlane_b32 s0, v75, 48
	s_nop 1
	v_cmp_gt_f32_e32 vcc, s0, v75
	v_cmp_eq_f32_e64 s[0:1], s0, v75
	s_and_b64 s[0:1], s[18:19], s[0:1]
	s_or_b64 s[0:1], vcc, s[0:1]
	v_cndmask_b32_e64 v82, 0, 1, s[0:1]
	v_readlane_b32 s0, v75, 56
	s_nop 1
	v_cmp_gt_f32_e32 vcc, s0, v75
	s_nop 1
	v_cndmask_b32_e64 v75, 0, 1, vcc
	v_add_u32_e32 v75, v77, v75
	v_add3_u32 v75, v75, v76, v78
	v_add3_u32 v75, v75, v79, v80
	v_add3_u32 v75, v75, v81, v82
	v_cmp_gt_u32_e32 vcc, 4, v75
	s_nop 1
	v_cndmask_b32_e32 v75, v174, v74, vcc
	v_mov_b32_e32 v74, 0
	s_mov_b32 s33, 0

; __device__ __forceinline__ void phase_ln_router(const Frame& F, const Args& a, int layer) {
;     ...
;             const bool gsel = grank < 4; const float cand = gsel ? bsd : -INFINITY; int rank = 0;
; #pragma unroll 8
;             for (int e2 = 0; e2 < 64; ++e2) { const float ov = __builtin_bit_cast(float, __builtin_amdgcn_readlane(__builtin_bit_cast(int, cand), e2)); rank += (ov > cand || (ov == cand && e2 < F.lane)) ? 1 : 0; }
;             const bool sel = gsel && rank < TOPK;
;             const float wsum = wave_sum(sel ? sg : 0.f);
;             if (sel) { SE[row * 8 + rank] = F.lane; SW[row * 8 + rank] = sg / wsum * 2.5f; mycnt += 1; } }
.LBB0_3076:
	v_cmp_gt_u32_e64 s[0:1], 8, v74
	s_and_b64 vcc, vcc, s[0:1]
	v_cndmask_b32_e32 v75, 0, v73, vcc
	s_waitcnt lgkmcnt(0)
	s_nop 1
	v_add_f32_dpp v75, v75, v75 quad_perm:[1,0,3,2] row_mask:0xf bank_mask:0xf
	s_waitcnt lgkmcnt(0)
	s_nop 1
	v_add_f32_dpp v75, v75, v75 quad_perm:[2,3,0,1] row_mask:0xf bank_mask:0xf
	s_waitcnt lgkmcnt(0)
	s_nop 1
	v_add_f32_dpp v75, v75, v75 row_half_mirror row_mask:0xf bank_mask:0xf
	s_waitcnt lgkmcnt(0)
	s_nop 1
	v_add_f32_dpp v75, v75, v75 row_mirror row_mask:0xf bank_mask:0xf
	ds_bpermute_b32 v76, v71, v75
	s_waitcnt lgkmcnt(0)
	v_add_f32_e32 v75, v75, v76
	ds_bpermute_b32 v76, v72, v75
	s_and_saveexec_b64 s[0:1], vcc
	s_cbranch_execz .LBB0_3078
	s_add_i32 s28, s22, s2
	s_waitcnt lgkmcnt(0)
	v_add_f32_e32 v78, v75, v76
	v_lshl_or_b32 v74, s28, 3, v74
	v_div_scale_f32 v79, s[28:29], v78, v78, v73
	v_rcp_f32_e32 v80, v79
	v_ashrrev_i32_e32 v75, 31, v74
	v_lshlrev_b64 v[74:75], 2, v[74:75]
	v_lshl_add_u64 v[76:77], s[24:25], 0, v[74:75]
	global_store_dword v[76:77], v1, off
	v_fma_f32 v76, -v79, v80, 1.0
	v_fmac_f32_e32 v80, v76, v80
	v_div_scale_f32 v76, vcc, v73, v78, v73
	v_mul_f32_e32 v77, v76, v80
	v_fma_f32 v81, -v79, v77, v76
	v_fmac_f32_e32 v77, v81, v80
	v_fma_f32 v76, -v79, v77, v76
	v_div_fmas_f32 v76, v76, v80, v77
	v_div_fixup_f32 v73, v76, v78, v73
	v_mul_f32_e32 v73, 0x40200000, v73
	v_lshl_add_u64 v[74:75], s[26:27], 0, v[74:75]
	v_add_u32_e32 v66, 1, v66
	global_store_dword v[74:75], v73, off
